# P10/P16 rms row loops: gain vector loaded once before the loop into dedicated registers instead of 16 loads per row
# speedup vs baseline: 1.0091x; 1.0091x over previous
.LBB0_1242:
	s_cmp_gt_i32 s90, 10
	s_cselect_b64 s[0:1], -1, 0
	s_cmp_lt_i32 s91, 11
	s_cselect_b64 s[2:3], -1, 0
	s_or_b64 s[0:1], s[0:1], s[2:3]
	s_and_b64 vcc, exec, s[0:1]
	s_cbranch_vccnz .LBB0_1311
	s_load_dwordx4 s[12:15], s[86:87], 0x88
	s_load_dwordx2 s[2:3], s[86:87], 0xc0
	s_lshl_b32 s0, s94, 3
	v_readlane_b32 s1, v245, 7
	s_add_i32 s4, s1, s0
	s_lshl_b32 s0, s96, 3
	s_cmpk_gt_i32 s4, 0x1fff
	s_waitcnt vmcnt(0) lgkmcnt(0)
	v_mov_b32_e32 v3, 0
	v_cmp_eq_u32_e64 s[6:7], 0, v194
	s_cbranch_scc1 .LBB0_1248
	s_load_dwordx2 s[8:9], s[86:87], 0x68
	v_mbcnt_lo_u32_b32 v1, -1, 0
	v_mbcnt_hi_u32_b32 v30, -1, v1
	v_lshlrev_b32_e32 v2, 4, v194
	v_and_b32_e32 v1, 64, v30
	s_waitcnt lgkmcnt(0)
	v_lshl_add_u64 v[4:5], s[8:9], 0, v[2:3]
	s_mov_b64 s[8:9], 0x1400
	v_add_u32_e32 v31, 64, v1
	v_xor_b32_e32 v1, 1, v30
	v_lshl_add_u64 v[8:9], v[4:5], 0, s[8:9]
	s_mov_b64 s[8:9], 0x1800
	v_cmp_lt_i32_e32 vcc, v1, v31
	v_xor_b32_e32 v2, 2, v30
	v_lshl_add_u64 v[10:11], v[4:5], 0, s[8:9]
	s_mov_b64 s[8:9], 0x1c00
	v_cndmask_b32_e32 v1, v30, v1, vcc
	v_cmp_lt_i32_e32 vcc, v2, v31
	v_xor_b32_e32 v32, 4, v30
	v_lshl_add_u64 v[12:13], v[4:5], 0, s[8:9]
	s_mov_b64 s[8:9], 0x2000
	v_cndmask_b32_e32 v2, v30, v2, vcc
	v_cmp_lt_i32_e32 vcc, v32, v31
	v_lshl_add_u64 v[14:15], v[4:5], 0, s[8:9]
	s_mov_b64 s[8:9], 0x2400
	v_cndmask_b32_e32 v32, v30, v32, vcc
	v_lshl_add_u64 v[16:17], v[4:5], 0, s[8:9]
	s_mov_b64 s[8:9], 0x2800
	v_lshlrev_b32_e32 v106, 2, v32
	v_xor_b32_e32 v32, 8, v30
	v_lshl_add_u64 v[18:19], v[4:5], 0, s[8:9]
	s_mov_b64 s[8:9], 0x2c00
	v_cmp_lt_i32_e32 vcc, v32, v31
	v_lshl_add_u64 v[20:21], v[4:5], 0, s[8:9]
	s_mov_b64 s[8:9], 0x3000
	v_cndmask_b32_e32 v32, v30, v32, vcc
	v_lshl_add_u64 v[22:23], v[4:5], 0, s[8:9]
	s_mov_b64 s[8:9], 0x3400
	v_lshlrev_b32_e32 v107, 2, v32
	v_xor_b32_e32 v32, 16, v30
	v_lshl_add_u64 v[24:25], v[4:5], 0, s[8:9]
	s_mov_b64 s[8:9], 0x3800
	v_cmp_lt_i32_e32 vcc, v32, v31
	v_lshl_add_u64 v[26:27], v[4:5], 0, s[8:9]
	s_mov_b64 s[8:9], 0x3c00
	v_cndmask_b32_e32 v32, v30, v32, vcc
	s_ashr_i32 s5, s4, 31
	v_lshl_add_u64 v[28:29], v[4:5], 0, s[8:9]
	v_lshlrev_b32_e32 v108, 2, v32
	v_xor_b32_e32 v32, 32, v30
	s_lshl_b64 s[8:9], s[4:5], 2
	v_cmp_lt_i32_e32 vcc, v32, v31
	s_add_u32 s22, s8, 0xf240000
	s_addc_u32 s23, s9, 0
	v_cndmask_b32_e32 v30, v30, v32, vcc
	s_lshl_b64 s[8:9], s[4:5], 13
	s_mov_b64 s[10:11], 0x1000
	v_lshlrev_b32_e32 v109, 2, v30
	s_ashr_i32 s1, s0, 31
	v_lshl_or_b32 v30, v194, 3, s8
	v_mov_b32_e32 v31, s9
	s_lshl_b64 s[8:9], s[4:5], 12
	v_lshl_add_u64 v[6:7], v[4:5], 0, s[10:11]
	v_lshlrev_b32_e32 v1, 2, v1
	v_lshlrev_b32_e32 v2, 2, v2
	s_lshl_b64 s[10:11], s[0:1], 2
	s_lshl_b64 s[16:17], s[0:1], 13
	v_lshl_or_b32 v32, v194, 2, s8
	v_mov_b32_e32 v33, s9
	s_lshl_b64 s[20:21], s[0:1], 12
	s_mov_b32 s1, 0x13401000
	v_mov_b32_e32 v110, 0x358637bd
	s_mov_b32 s5, 0xf800000
	v_mov_b32_e32 v111, 0x260
	s_mov_b32 s24, 0x42fe0000
	s_mov_b32 s25, 0x40c0c00
	s_mov_b32 s26, 0x37400000
	s_mov_b32 s27, s4
	global_load_dwordx4 v[196:199], v[4:5], off offset:1024
	global_load_dwordx4 v[200:203], v[4:5], off offset:2048
	global_load_dwordx4 v[204:207], v[4:5], off offset:3072
	global_load_dwordx4 v[208:211], v[4:5], off
	global_load_dwordx4 v[212:215], v[6:7], off
	global_load_dwordx4 v[216:219], v[8:9], off
	global_load_dwordx4 v[220:223], v[10:11], off
	global_load_dwordx4 v[224:227], v[12:13], off
	global_load_dwordx4 v[228:231], v[14:15], off
	global_load_dwordx4 v[232:235], v[16:17], off
	global_load_dwordx4 v[236:239], v[18:19], off
	global_load_dwordx4 v[240:243], v[20:21], off
	global_load_dwordx4 v[156:159], v[22:23], off
	global_load_dwordx4 v[160:163], v[24:25], off
	global_load_dwordx4 v[164:167], v[26:27], off
	global_load_dwordx4 v[168:171], v[28:29], off
	s_branch .LBB0_1246

; __device__ __forceinline__ void rms_row_i8_b(const bf16_t* xrow, const float* gain, unsigned char* qrow, float* qscale, int lane) {
;     const u32x2* xr = (const u32x2*)xrow + lane; const f32x4* gr = (const f32x4*)gain + lane;
;     f32x4 v[16]; float s = 0.f;
; #pragma unroll
;     for (int j = 0; j < 16; ++j) { { const u32x2 q = xr[64 * j]; v[j] = (f32x4){bflo(q.x), bfhi(q.x), bflo(q.y), bfhi(q.y)}; } s += (v[j].x * v[j].x + v[j].y * v[j].y) + (v[j].z * v[j].z + v[j].w * v[j].w); }
;     const float rstd = 1.f / sqrtf(wave_sum(s) * (1.f / D) + RMS_EPS);
.LBB0_1246:
	v_lshl_add_u64 v[34:35], s[88:89], 0, v[30:31]
	v_add_co_u32_e32 v36, vcc, 0x13400000, v34
	s_nop 1
	v_addc_co_u32_e32 v37, vcc, 0, v35, vcc
	global_load_dwordx2 v[38:39], v[36:37], off
	global_load_dwordx2 v[40:41], v[36:37], off offset:512
	global_load_dwordx2 v[42:43], v[36:37], off offset:1024
	global_load_dwordx2 v[44:45], v[36:37], off offset:1536
	global_load_dwordx2 v[46:47], v[36:37], off offset:2048
	global_load_dwordx2 v[48:49], v[36:37], off offset:2560
	global_load_dwordx2 v[50:51], v[36:37], off offset:3072
	global_load_dwordx2 v[52:53], v[36:37], off offset:3584
	v_add_co_u32_e32 v34, vcc, s1, v34
	s_waitcnt vmcnt(7)
	v_and_b32_e32 v103, 0xffff0000, v38
	v_addc_co_u32_e32 v35, vcc, 0, v35, vcc
	global_load_dwordx2 v[54:55], v[34:35], off
	global_load_dwordx2 v[56:57], v[34:35], off offset:512
	global_load_dwordx2 v[62:63], v[34:35], off offset:1024
	global_load_dwordx2 v[64:65], v[34:35], off offset:1536
	global_load_dwordx2 v[66:67], v[34:35], off offset:2048
	global_load_dwordx2 v[72:73], v[34:35], off offset:2560
	global_load_dwordx2 v[74:75], v[34:35], off offset:3072
	global_load_dwordx2 v[112:113], v[34:35], off offset:3584
	v_and_b32_e32 v105, 0xffff0000, v39
	v_lshlrev_b32_e32 v102, 16, v38
	v_lshlrev_b32_e32 v104, 16, v39
	s_waitcnt vmcnt(14)
	v_and_b32_e32 v101, 0xffff0000, v41
	v_and_b32_e32 v100, 0xffff0000, v40
	s_waitcnt vmcnt(13)
	v_and_b32_e32 v95, 0xffff0000, v42
	s_waitcnt vmcnt(12)
	v_lshlrev_b32_e32 v93, 16, v44
	s_waitcnt vmcnt(8)
	v_lshlrev_b32_e32 v39, 16, v52
	v_and_b32_e32 v37, 0xffff0000, v52
	v_mul_f32_e32 v36, v105, v105
	v_mul_f32_e32 v38, v103, v103
	v_lshlrev_b32_e32 v99, 16, v41
	v_lshlrev_b32_e32 v98, 16, v40
	v_lshlrev_b32_e32 v94, 16, v42
	v_lshlrev_b32_e32 v96, 16, v43
	v_and_b32_e32 v97, 0xffff0000, v43
	v_and_b32_e32 v91, 0xffff0000, v44
	v_lshlrev_b32_e32 v88, 16, v45
	v_and_b32_e32 v89, 0xffff0000, v45
	v_lshlrev_b32_e32 v81, 16, v47
	v_lshlrev_b32_e32 v80, 16, v46
	v_and_b32_e32 v83, 0xffff0000, v47
	v_and_b32_e32 v82, 0xffff0000, v46
	v_lshlrev_b32_e32 v47, 16, v49
	v_lshlrev_b32_e32 v46, 16, v48
	v_and_b32_e32 v45, 0xffff0000, v49
	v_and_b32_e32 v44, 0xffff0000, v48
	v_lshlrev_b32_e32 v42, 16, v50
	v_and_b32_e32 v43, 0xffff0000, v50
	v_lshlrev_b32_e32 v40, 16, v51
	v_and_b32_e32 v41, 0xffff0000, v51
	v_pk_mul_f32 v[48:49], v[100:101], v[100:101]
	v_mov_b32_e32 v51, v93
	v_mul_f32_e32 v50, v95, v95
	v_pk_fma_f32 v[68:69], v[104:105], v[104:105], v[36:37] op_sel_hi:[1,1,0]
	v_pk_fma_f32 v[70:71], v[102:103], v[102:103], v[38:39] op_sel_hi:[1,1,0]
	v_mul_f32_e32 v52, v97, v97
	v_pk_fma_f32 v[48:49], v[98:99], v[98:99], v[48:49]
	v_pk_fma_f32 v[76:77], v[94:95], v[94:95], v[50:51] op_sel_hi:[1,1,0]
	v_mov_b32_e32 v92, v70
	v_mov_b32_e32 v50, v68
	v_lshlrev_b32_e32 v34, 16, v53
	v_and_b32_e32 v35, 0xffff0000, v53
	v_mul_f32_e32 v78, v91, v91
	v_mul_f32_e32 v79, v88, v88
	v_mul_f32_e32 v84, v89, v89
	v_pk_fma_f32 v[52:53], v[96:97], v[96:97], v[52:53] op_sel_hi:[1,1,0]
	v_pk_add_f32 v[68:69], v[70:71], v[68:69]
	v_pk_add_f32 v[48:49], v[48:49], v[48:49] op_sel:[0,1] op_sel_hi:[1,0]
	v_pk_mul_f32 v[50:51], v[92:93], v[50:51]
	v_mov_b32_e32 v77, v79
	v_mov_b32_e32 v53, v84
	v_mov_b32_e32 v49, v78
	v_mov_b32_e32 v69, v51
	v_pk_mul_f32 v[58:59], v[82:83], v[82:83]
	v_pk_add_f32 v[52:53], v[76:77], v[52:53]
	v_pk_add_f32 v[48:49], v[68:69], v[48:49]
	v_pk_fma_f32 v[58:59], v[80:81], v[80:81], v[58:59]
	v_pk_add_f32 v[48:49], v[48:49], v[52:53]
	v_pk_add_f32 v[58:59], v[58:59], v[58:59] op_sel:[0,1] op_sel_hi:[1,0]
	v_pk_add_f32 v[48:49], v[48:49], v[48:49] op_sel:[0,1] op_sel_hi:[1,0]
	v_pk_mul_f32 v[60:61], v[44:45], v[44:45]
	v_mov_b32_e32 v38, v48
	v_mov_b32_e32 v50, v58
	v_mov_b32_e32 v51, v39
	v_pk_fma_f32 v[60:61], v[46:47], v[46:47], v[60:61]
	v_pk_add_f32 v[48:49], v[48:49], v[58:59]
	v_pk_mul_f32 v[50:51], v[38:39], v[50:51]
	v_mul_f32_e32 v85, v37, v37
	v_mov_b32_e32 v49, v51
	v_pk_add_f32 v[50:51], v[60:61], v[60:61] op_sel:[0,1] op_sel_hi:[1,0]
	v_mul_f32_e32 v36, v43, v43
	v_mov_b32_e32 v51, v85
	v_pk_add_f32 v[48:49], v[48:49], v[50:51]
	v_pk_fma_f32 v[50:51], v[42:43], v[42:43], v[36:37] op_sel_hi:[1,1,0]
	v_mul_f32_e32 v36, v41, v41
	v_mul_f32_e32 v86, v34, v34
	v_mul_f32_e32 v68, v35, v35
	v_pk_fma_f32 v[52:53], v[40:41], v[40:41], v[36:37] op_sel_hi:[1,1,0]
	v_mov_b32_e32 v51, v86
	v_mov_b32_e32 v53, v68
	v_pk_add_f32 v[50:51], v[50:51], v[52:53]
	s_waitcnt vmcnt(7)
	v_and_b32_e32 v71, 0xffff0000, v55
	v_and_b32_e32 v70, 0xffff0000, v54
	v_pk_add_f32 v[76:77], v[48:49], v[50:51]
	v_lshlrev_b32_e32 v69, 16, v55
	v_lshlrev_b32_e32 v68, 16, v54
	v_pk_mul_f32 v[48:49], v[70:71], v[70:71]
	s_waitcnt vmcnt(6)
	v_and_b32_e32 v61, 0xffff0000, v57
	v_pk_fma_f32 v[48:49], v[68:69], v[68:69], v[48:49]
	v_and_b32_e32 v60, 0xffff0000, v56
	v_pk_add_f32 v[78:79], v[48:49], v[48:49] op_sel:[0,1] op_sel_hi:[1,0]
	v_lshlrev_b32_e32 v59, 16, v57
	v_lshlrev_b32_e32 v58, 16, v56
	v_pk_mul_f32 v[48:49], v[60:61], v[60:61]
	s_waitcnt vmcnt(5)
	v_lshlrev_b32_e32 v54, 16, v62
	v_and_b32_e32 v55, 0xffff0000, v62
	v_lshlrev_b32_e32 v56, 16, v63
	v_and_b32_e32 v57, 0xffff0000, v63
	s_waitcnt vmcnt(4)
	v_lshlrev_b32_e32 v53, 16, v64
	v_pk_add_f32 v[62:63], v[76:77], v[76:77] op_sel:[0,1] op_sel_hi:[1,0]
	v_pk_fma_f32 v[84:85], v[58:59], v[58:59], v[48:49]
	v_and_b32_e32 v51, 0xffff0000, v64
	v_lshlrev_b32_e32 v48, 16, v65
	v_and_b32_e32 v49, 0xffff0000, v65
	v_mov_b32_e32 v52, v62
	v_mov_b32_e32 v64, v78
	v_mov_b32_e32 v65, v53
	v_pk_add_f32 v[62:63], v[62:63], v[78:79]
	v_pk_mul_f32 v[64:65], v[52:53], v[64:65]
	v_mul_f32_e32 v36, v51, v51
	v_mov_b32_e32 v63, v65
	v_pk_add_f32 v[64:65], v[84:85], v[84:85] op_sel:[0,1] op_sel_hi:[1,0]
	v_mul_f32_e32 v38, v48, v48
	v_mov_b32_e32 v65, v36
	v_mul_f32_e32 v36, v55, v55
	v_pk_add_f32 v[62:63], v[62:63], v[64:65]
	v_pk_fma_f32 v[64:65], v[54:55], v[54:55], v[36:37] op_sel_hi:[1,1,0]
	v_mul_f32_e32 v36, v57, v57
	v_mul_f32_e32 v50, v49, v49
	v_pk_fma_f32 v[76:77], v[56:57], v[56:57], v[36:37] op_sel_hi:[1,1,0]
	v_mov_b32_e32 v65, v38
	v_mov_b32_e32 v77, v50
	v_pk_add_f32 v[64:65], v[64:65], v[76:77]
	s_waitcnt vmcnt(3)
; __device__ __forceinline__ void rms_row_i8_b(const bf16_t* xrow, const float* gain, unsigned char* qrow, float* qscale, int lane) {
;     ...
;     for (int j = 0; j < 16; ++j) { { const u32x2 q = xr[64 * j]; v[j] = (f32x4){bflo(q.x), bfhi(q.x), bflo(q.y), bfhi(q.y)}; } s += (v[j].x * v[j].x + v[j].y * v[j].y) + (v[j].z * v[j].z + v[j].w * v[j].w); }
;     const float rstd = 1.f / sqrtf(wave_sum(s) * (1.f / D) + RMS_EPS);
;     float amax = 0.f;
; #pragma unroll
;     for (int j = 0; j < 16; ++j) { v[j] = v[j] * rstd * gr[64 * j]; amax = fmaxf(fmaxf(amax, fmaxf(fabsf(v[j].x), fabsf(v[j].y))), fmaxf(fabsf(v[j].z), fabsf(v[j].w))); }
	v_and_b32_e32 v87, 0xffff0000, v67
	v_and_b32_e32 v86, 0xffff0000, v66
	v_pk_add_f32 v[114:115], v[62:63], v[64:65]
	v_lshlrev_b32_e32 v85, 16, v67
	v_lshlrev_b32_e32 v84, 16, v66
	v_pk_mul_f32 v[62:63], v[86:87], v[86:87]
	s_waitcnt vmcnt(2)
	v_and_b32_e32 v79, 0xffff0000, v73
	v_pk_fma_f32 v[62:63], v[84:85], v[84:85], v[62:63]
	v_and_b32_e32 v78, 0xffff0000, v72
	v_pk_add_f32 v[116:117], v[62:63], v[62:63] op_sel:[0,1] op_sel_hi:[1,0]
	v_lshlrev_b32_e32 v77, 16, v73
	v_lshlrev_b32_e32 v76, 16, v72
	v_pk_mul_f32 v[62:63], v[78:79], v[78:79]
	s_waitcnt vmcnt(0)
	v_lshlrev_b32_e32 v67, 16, v112
	v_pk_fma_f32 v[118:119], v[76:77], v[76:77], v[62:63]
	v_and_b32_e32 v65, 0xffff0000, v112
	v_lshlrev_b32_e32 v62, 16, v113
	v_and_b32_e32 v63, 0xffff0000, v113
	v_pk_add_f32 v[112:113], v[114:115], v[114:115] op_sel:[0,1] op_sel_hi:[1,0]
	v_mov_b32_e32 v114, v116
	v_mov_b32_e32 v66, v112
	v_mov_b32_e32 v115, v67
	v_pk_add_f32 v[112:113], v[112:113], v[116:117]
	v_pk_mul_f32 v[114:115], v[66:67], v[114:115]
	v_and_b32_e32 v73, 0xffff0000, v74
	v_mul_f32_e32 v36, v65, v65
	v_mov_b32_e32 v113, v115
	v_pk_add_f32 v[114:115], v[118:119], v[118:119] op_sel:[0,1] op_sel_hi:[1,0]
	v_lshlrev_b32_e32 v72, 16, v74
	v_lshlrev_b32_e32 v74, 16, v75
	v_and_b32_e32 v75, 0xffff0000, v75
	v_mov_b32_e32 v115, v36
	v_mul_f32_e32 v36, v73, v73
	v_pk_add_f32 v[112:113], v[112:113], v[114:115]
	v_pk_fma_f32 v[114:115], v[72:73], v[72:73], v[36:37] op_sel_hi:[1,1,0]
	v_mul_f32_e32 v36, v75, v75
	v_mul_f32_e32 v38, v62, v62
	v_mul_f32_e32 v50, v63, v63
	v_pk_fma_f32 v[116:117], v[74:75], v[74:75], v[36:37] op_sel_hi:[1,1,0]
	v_mov_b32_e32 v115, v38
	v_mov_b32_e32 v117, v50
	v_pk_add_f32 v[114:115], v[114:115], v[116:117]
	v_pk_add_f32 v[112:113], v[112:113], v[114:115]
	v_add_f32_e32 v36, v112, v113
	ds_bpermute_b32 v38, v1, v36
	s_waitcnt lgkmcnt(0)
	v_add_f32_e32 v36, v36, v38
	ds_bpermute_b32 v38, v2, v36
	v_mov_b32_e32 v90, v93
	v_mov_b32_e32 v92, v80
	v_mov_b32_e32 v93, v82
	s_waitcnt lgkmcnt(0)
	v_add_f32_e32 v36, v36, v38
	ds_bpermute_b32 v38, v106, v36
	v_mov_b32_e32 v82, v81
	s_waitcnt lgkmcnt(0)
	v_add_f32_e32 v36, v36, v38
	ds_bpermute_b32 v38, v107, v36
	s_waitcnt lgkmcnt(0)
	v_add_f32_e32 v36, v36, v38
	ds_bpermute_b32 v38, v108, v36
	s_waitcnt lgkmcnt(0)
	v_add_f32_e32 v36, v36, v38
	ds_bpermute_b32 v38, v109, v36
	s_waitcnt lgkmcnt(0)
	v_add_f32_e32 v36, v36, v38
	v_fmamk_f32 v36, v36, 0x39800000, v110
	v_mul_f32_e32 v38, 0x4f800000, v36
	v_cmp_gt_f32_e32 vcc, s5, v36
	s_nop 1
	v_cndmask_b32_e32 v36, v36, v38, vcc
	v_sqrt_f32_e32 v38, v36
	s_nop 0
	v_add_u32_e32 v50, -1, v38
	v_fma_f32 v52, -v50, v38, v36
	v_cmp_ge_f32_e64 s[8:9], 0, v52
	v_add_u32_e32 v52, 1, v38
	s_nop 0
	v_cndmask_b32_e64 v50, v38, v50, s[8:9]
	v_fma_f32 v38, -v52, v38, v36
	v_cmp_lt_f32_e64 s[8:9], 0, v38
	s_nop 1
	v_cndmask_b32_e64 v38, v50, v52, s[8:9]
	v_mul_f32_e32 v50, 0x37800000, v38
	v_cndmask_b32_e32 v38, v38, v50, vcc
	v_cmp_class_f32_e32 vcc, v36, v111
	s_nop 1
	v_cndmask_b32_e32 v36, v38, v36, vcc
	v_div_scale_f32 v38, s[8:9], v36, v36, 1.0
	v_rcp_f32_e32 v50, v38
	s_nop 0
	v_fma_f32 v52, -v38, v50, 1.0
	v_fmac_f32_e32 v50, v52, v50
	v_div_scale_f32 v52, vcc, 1.0, v36, 1.0
	v_mul_f32_e32 v64, v52, v50
	v_fma_f32 v66, -v38, v64, v52
	v_fmac_f32_e32 v64, v66, v50
	v_fma_f32 v38, -v38, v64, v52
	v_div_fmas_f32 v38, v38, v50, v64
	v_div_fixup_f32 v66, v38, v36, 1.0
	v_pk_mul_f32 v[148:149], v[66:67], v[102:103] op_sel_hi:[0,1]
	v_pk_mul_f32 v[102:103], v[66:67], v[104:105] op_sel_hi:[0,1]
	s_waitcnt vmcnt(5)
	v_pk_mul_f32 v[102:103], v[210:211], v[102:103]
	v_pk_mul_f32 v[104:105], v[208:209], v[148:149]
	v_mov_b32_e32 v148, v98
	v_mov_b32_e32 v149, v100
	v_mov_b32_e32 v100, v99
	v_pk_mul_f32 v[148:149], v[66:67], v[148:149] op_sel_hi:[0,1]
	v_pk_mul_f32 v[98:99], v[66:67], v[100:101] op_sel_hi:[0,1]
	v_pk_mul_f32 v[98:99], v[198:199], v[98:99]
	v_pk_mul_f32 v[100:101], v[196:197], v[148:149]
	v_pk_mul_f32 v[148:149], v[66:67], v[94:95] op_sel_hi:[0,1]
	v_pk_mul_f32 v[94:95], v[66:67], v[96:97] op_sel_hi:[0,1]
	v_pk_mul_f32 v[94:95], v[202:203], v[94:95]
	v_pk_mul_f32 v[96:97], v[200:201], v[148:149]
	v_pk_mul_f32 v[90:91], v[90:91], v[66:67] op_sel_hi:[1,0]
	v_pk_mul_f32 v[88:89], v[88:89], v[66:67] op_sel_hi:[1,0]
	v_pk_mul_f32 v[90:91], v[204:205], v[90:91]
	v_pk_mul_f32 v[88:89], v[206:207], v[88:89]
	v_pk_mul_f32 v[92:93], v[66:67], v[92:93] op_sel_hi:[0,1]
	v_pk_mul_f32 v[80:81], v[66:67], v[82:83] op_sel_hi:[0,1]
	s_waitcnt vmcnt(8)
	v_pk_mul_f32 v[80:81], v[214:215], v[80:81]
	v_pk_mul_f32 v[82:83], v[212:213], v[92:93]
	v_mov_b32_e32 v92, v46
	v_mov_b32_e32 v93, v44
	v_mov_b32_e32 v44, v47
	v_pk_mul_f32 v[92:93], v[66:67], v[92:93] op_sel_hi:[0,1]
	v_pk_mul_f32 v[44:45], v[66:67], v[44:45] op_sel_hi:[0,1]
	s_waitcnt vmcnt(9)
	v_pk_mul_f32 v[152:153], v[218:219], v[44:45]
	v_pk_mul_f32 v[92:93], v[216:217], v[92:93]
	v_max_f32_e64 v36, |v104|, |v105|
	v_max_f32_e64 v38, |v102|, |v103|
	v_max3_f32 v36, v36, 0, v38
	v_max_f32_e64 v38, |v100|, |v101|
	v_max_f32_e64 v50, |v98|, |v99|
	v_max3_f32 v36, v36, v38, v50
	v_max_f32_e64 v38, |v96|, |v97|
	v_max_f32_e64 v50, |v94|, |v95|
	v_max3_f32 v36, v36, v38, v50
	v_max_f32_e64 v38, |v90|, |v91|
	v_max_f32_e64 v50, |v88|, |v89|
	v_max3_f32 v36, v36, v38, v50
	v_max_f32_e64 v38, |v82|, |v83|
	v_max_f32_e64 v50, |v80|, |v81|
	v_pk_mul_f32 v[42:43], v[66:67], v[42:43] op_sel_hi:[0,1]
	v_pk_mul_f32 v[40:41], v[66:67], v[40:41] op_sel_hi:[0,1]
	v_max3_f32 v36, v36, v38, v50
	v_max_f32_e64 v38, |v92|, |v93|
	v_max_f32_e64 v44, |v152|, |v153|
	s_waitcnt vmcnt(9)
; __device__ __forceinline__ void rms_row_i8_b(const bf16_t* xrow, const float* gain, unsigned char* qrow, float* qscale, int lane) {
;     ...
;     for (int j = 0; j < 16; ++j) { v[j] = v[j] * rstd * gr[64 * j]; amax = fmaxf(fmaxf(amax, fmaxf(fabsf(v[j].x), fabsf(v[j].y))), fmaxf(fabsf(v[j].z), fabsf(v[j].w))); }
; #pragma unroll
;     for (int o = 1; o < 64; o <<= 1) amax = fmaxf(amax, __shfl_xor(amax, o));
;     const float scale = amax > 0.f ? 127.f / amax : 0.f;
; #pragma unroll
;     for (int j = 0; j < 16; ++j) ((unsigned*)qrow)[lane + 64 * j] = pack_i8x4(v[j].x * scale, v[j].y * scale, v[j].z * scale, v[j].w * scale);
	v_pk_mul_f32 v[138:139], v[222:223], v[40:41]
	v_pk_mul_f32 v[136:137], v[220:221], v[42:43]
	v_max3_f32 v36, v36, v38, v44
	v_max_f32_e64 v38, |v136|, |v137|
	v_max_f32_e64 v40, |v138|, |v139|
	v_max3_f32 v38, v36, v38, v40
	v_mov_b32_e32 v36, v39
	v_pk_mul_f32 v[36:37], v[36:37], v[66:67] op_sel_hi:[1,0]
	v_pk_mul_f32 v[34:35], v[34:35], v[66:67] op_sel_hi:[1,0]
	s_waitcnt vmcnt(8)
	v_pk_mul_f32 v[140:141], v[224:225], v[36:37]
	v_pk_mul_f32 v[142:143], v[226:227], v[34:35]
	v_max_f32_e64 v34, |v140|, |v141|
	v_max_f32_e64 v35, |v142|, |v143|
	v_max3_f32 v38, v38, v34, v35
	v_mov_b32_e32 v34, v68
	v_mov_b32_e32 v35, v70
	v_mov_b32_e32 v70, v69
	v_pk_mul_f32 v[34:35], v[66:67], v[34:35] op_sel_hi:[0,1]
	v_pk_mul_f32 v[36:37], v[66:67], v[70:71] op_sel_hi:[0,1]
	s_waitcnt vmcnt(7)
	v_pk_mul_f32 v[70:71], v[230:231], v[36:37]
	v_pk_mul_f32 v[144:145], v[228:229], v[34:35]
	v_max_f32_e64 v35, |v70|, |v71|
	v_max_f32_e64 v34, |v144|, |v145|
	v_max3_f32 v38, v38, v34, v35
	v_mov_b32_e32 v34, v58
	v_mov_b32_e32 v35, v60
	v_mov_b32_e32 v60, v59
	v_pk_mul_f32 v[34:35], v[66:67], v[34:35] op_sel_hi:[0,1]
	v_pk_mul_f32 v[36:37], v[66:67], v[60:61] op_sel_hi:[0,1]
	s_waitcnt vmcnt(6)
	v_pk_mul_f32 v[60:61], v[234:235], v[36:37]
	v_pk_mul_f32 v[68:69], v[232:233], v[34:35]
	v_max_f32_e64 v35, |v60|, |v61|
	v_max_f32_e64 v34, |v68|, |v69|
	v_max3_f32 v38, v38, v34, v35
	v_pk_mul_f32 v[34:35], v[66:67], v[54:55] op_sel_hi:[0,1]
	v_pk_mul_f32 v[36:37], v[66:67], v[56:57] op_sel_hi:[0,1]
	s_waitcnt vmcnt(5)
	v_pk_mul_f32 v[56:57], v[238:239], v[36:37]
	v_pk_mul_f32 v[58:59], v[236:237], v[34:35]
	v_max_f32_e64 v35, |v56|, |v57|
	v_max_f32_e64 v34, |v58|, |v59|
	v_mov_b32_e32 v50, v53
	v_max3_f32 v38, v38, v34, v35
	v_pk_mul_f32 v[34:35], v[50:51], v[66:67] op_sel_hi:[1,0]
	v_pk_mul_f32 v[36:37], v[48:49], v[66:67] op_sel_hi:[1,0]
	s_waitcnt vmcnt(4)
	v_pk_mul_f32 v[52:53], v[34:35], v[240:241]
	v_pk_mul_f32 v[50:51], v[36:37], v[242:243]
	v_max_f32_e64 v34, |v52|, |v53|
	v_max_f32_e64 v35, |v50|, |v51|
	v_max3_f32 v38, v38, v34, v35
	v_mov_b32_e32 v34, v84
	v_mov_b32_e32 v35, v86
	v_mov_b32_e32 v86, v85
	v_pk_mul_f32 v[34:35], v[66:67], v[34:35] op_sel_hi:[0,1]
	v_pk_mul_f32 v[36:37], v[66:67], v[86:87] op_sel_hi:[0,1]
	s_waitcnt vmcnt(3)
	v_pk_mul_f32 v[46:47], v[36:37], v[158:159]
	v_pk_mul_f32 v[48:49], v[34:35], v[156:157]
	v_max_f32_e64 v35, |v46|, |v47|
	v_max_f32_e64 v34, |v48|, |v49|
	v_max3_f32 v38, v38, v34, v35
	v_mov_b32_e32 v34, v76
	v_mov_b32_e32 v35, v78
	v_mov_b32_e32 v78, v77
	v_pk_mul_f32 v[34:35], v[66:67], v[34:35] op_sel_hi:[0,1]
	v_pk_mul_f32 v[36:37], v[66:67], v[78:79] op_sel_hi:[0,1]
	s_waitcnt vmcnt(2)
	v_pk_mul_f32 v[42:43], v[36:37], v[162:163]
	v_pk_mul_f32 v[44:45], v[34:35], v[160:161]
	v_max_f32_e64 v35, |v42|, |v43|
	v_max_f32_e64 v34, |v44|, |v45|
	v_max3_f32 v54, v38, v34, v35
	v_pk_mul_f32 v[34:35], v[66:67], v[72:73] op_sel_hi:[0,1]
	v_pk_mul_f32 v[36:37], v[66:67], v[74:75] op_sel_hi:[0,1]
	s_waitcnt vmcnt(1)
	v_pk_mul_f32 v[38:39], v[36:37], v[166:167]
	v_pk_mul_f32 v[40:41], v[34:35], v[164:165]
	v_max_f32_e64 v35, |v38|, |v39|
	v_max_f32_e64 v34, |v40|, |v41|
	v_mov_b32_e32 v64, v67
	v_max3_f32 v54, v54, v34, v35
	v_pk_mul_f32 v[36:37], v[64:65], v[66:67] op_sel_hi:[1,0]
	v_pk_mul_f32 v[34:35], v[62:63], v[66:67] op_sel_hi:[1,0]
	s_waitcnt vmcnt(0)
	v_pk_mul_f32 v[36:37], v[36:37], v[168:169]
	v_pk_mul_f32 v[34:35], v[34:35], v[170:171]
	v_max_f32_e64 v55, |v36|, |v37|
	v_max_f32_e64 v62, |v34|, |v35|
	v_max3_f32 v54, v54, v55, v62
	ds_bpermute_b32 v55, v1, v54
	s_waitcnt lgkmcnt(0)
	v_max_f32_e32 v55, v55, v55
	v_max_f32_e32 v54, v54, v55
	ds_bpermute_b32 v55, v2, v54
	s_waitcnt lgkmcnt(0)
	v_max_f32_e32 v55, v55, v55
	v_max_f32_e32 v54, v54, v55
	ds_bpermute_b32 v55, v106, v54
	s_waitcnt lgkmcnt(0)
	v_max_f32_e32 v55, v55, v55
	v_max_f32_e32 v54, v54, v55
	ds_bpermute_b32 v55, v107, v54
	s_waitcnt lgkmcnt(0)
	v_max_f32_e32 v55, v55, v55
	v_max_f32_e32 v54, v54, v55
	ds_bpermute_b32 v55, v108, v54
	s_waitcnt lgkmcnt(0)
	v_max_f32_e32 v55, v55, v55
	v_max_f32_e32 v54, v54, v55
	ds_bpermute_b32 v55, v109, v54
	s_waitcnt lgkmcnt(0)
	v_max_f32_e32 v55, v55, v55
	v_max_f32_e32 v62, v54, v55
	v_div_scale_f32 v54, s[8:9], v62, v62, s24
	v_rcp_f32_e32 v55, v54
	s_nop 0
	v_fma_f32 v63, -v54, v55, 1.0
	v_fmac_f32_e32 v55, v63, v55
	v_div_scale_f32 v63, vcc, s24, v62, s24
	v_mul_f32_e32 v64, v63, v55
	v_fma_f32 v65, -v54, v64, v63
	v_fmac_f32_e32 v64, v65, v55
	v_fma_f32 v54, -v54, v64, v63
	v_div_fmas_f32 v54, v54, v55, v64
	v_div_fixup_f32 v54, v54, v62, s24
	v_cmp_lt_f32_e32 vcc, 0, v62
	s_nop 1
	v_cndmask_b32_e32 v63, 0, v54, vcc
	v_mul_f32_e32 v55, v105, v63
	v_mul_f32_e32 v54, v104, v63
	v_mul_f32_e32 v64, v102, v63
	v_mul_f32_e32 v65, v103, v63
	v_rndne_f32_e32 v55, v55
	v_rndne_f32_e32 v54, v54
	v_cvt_i32_f32_e32 v55, v55
	v_rndne_f32_e32 v64, v64
	v_rndne_f32_e32 v65, v65
	v_cvt_i32_f32_e32 v54, v54
	v_cvt_i32_f32_sdwa v64, v64 dst_sel:WORD_1 dst_unused:UNUSED_PAD src0_sel:DWORD
	v_cvt_i32_f32_e32 v65, v65
	v_lshlrev_b32_e32 v55, 8, v55
	v_and_b32_e32 v55, 0xff00, v55
	v_and_b32_e32 v64, 0xff0000, v64
	v_perm_b32 v54, v65, v54, s25
	v_or3_b32 v64, v54, v55, v64
	v_lshl_add_u64 v[54:55], s[88:89], 0, v[32:33]
	v_add_co_u32_e32 v54, vcc, s26, v54
	v_mul_f32_e32 v65, v101, v63
	s_nop 0
	v_addc_co_u32_e32 v55, vcc, 0, v55, vcc
	global_store_dword v[54:55], v64, off
	v_mul_f32_e32 v64, v100, v63
	v_mul_f32_e32 v66, v98, v63
	v_mul_f32_e32 v67, v99, v63
	v_rndne_f32_e32 v65, v65
	v_rndne_f32_e32 v64, v64
	v_cvt_i32_f32_e32 v65, v65
	v_rndne_f32_e32 v66, v66
	v_rndne_f32_e32 v67, v67
	v_cvt_i32_f32_e32 v64, v64
; __device__ __forceinline__ unsigned pack_i8x4(float a, float b, float c, float d) {
;     const int ia = (int)__builtin_rintf(a), ib = (int)__builtin_rintf(b), ic = (int)__builtin_rintf(c), id = (int)__builtin_rintf(d);
;     return ((unsigned)ia & 255u) | (((unsigned)ib & 255u) << 8) | (((unsigned)ic & 255u) << 16) | ((unsigned)id << 24);
; }
; __device__ __forceinline__ void rms_row_i8_b(const bf16_t* xrow, const float* gain, unsigned char* qrow, float* qscale, int lane) {
;     ...
; #pragma unroll
;     for (int j = 0; j < 16; ++j) ((unsigned*)qrow)[lane + 64 * j] = pack_i8x4(v[j].x * scale, v[j].y * scale, v[j].z * scale, v[j].w * scale);
	v_cvt_i32_f32_sdwa v66, v66 dst_sel:WORD_1 dst_unused:UNUSED_PAD src0_sel:DWORD
	v_cvt_i32_f32_e32 v67, v67
	v_lshlrev_b32_e32 v65, 8, v65
	v_and_b32_e32 v65, 0xff00, v65
	v_and_b32_e32 v66, 0xff0000, v66
	v_perm_b32 v64, v67, v64, s25
	v_or3_b32 v64, v64, v65, v66
	v_mul_f32_e32 v65, v97, v63
	global_store_dword v[54:55], v64, off offset:256
	v_mul_f32_e32 v64, v96, v63
	v_mul_f32_e32 v66, v94, v63
	v_mul_f32_e32 v67, v95, v63
	v_rndne_f32_e32 v65, v65
	v_rndne_f32_e32 v64, v64
	v_cvt_i32_f32_e32 v65, v65
	v_rndne_f32_e32 v66, v66
	v_rndne_f32_e32 v67, v67
	v_cvt_i32_f32_e32 v64, v64
	v_cvt_i32_f32_sdwa v66, v66 dst_sel:WORD_1 dst_unused:UNUSED_PAD src0_sel:DWORD
	v_cvt_i32_f32_e32 v67, v67
	v_lshlrev_b32_e32 v65, 8, v65
	v_and_b32_e32 v65, 0xff00, v65
	v_and_b32_e32 v66, 0xff0000, v66
	v_perm_b32 v64, v67, v64, s25
	v_or3_b32 v64, v64, v65, v66
	v_mul_f32_e32 v65, v91, v63
	global_store_dword v[54:55], v64, off offset:512
	v_mul_f32_e32 v64, v90, v63
	v_mul_f32_e32 v66, v88, v63
	v_mul_f32_e32 v67, v89, v63
	v_rndne_f32_e32 v65, v65
	v_rndne_f32_e32 v64, v64
	v_cvt_i32_f32_e32 v65, v65
	v_rndne_f32_e32 v66, v66
	v_rndne_f32_e32 v67, v67
	v_cvt_i32_f32_e32 v64, v64
	v_cvt_i32_f32_sdwa v66, v66 dst_sel:WORD_1 dst_unused:UNUSED_PAD src0_sel:DWORD
	v_cvt_i32_f32_e32 v67, v67
	v_lshlrev_b32_e32 v65, 8, v65
	v_and_b32_e32 v65, 0xff00, v65
	v_and_b32_e32 v66, 0xff0000, v66
	v_perm_b32 v64, v67, v64, s25
	v_or3_b32 v64, v64, v65, v66
	v_mul_f32_e32 v65, v83, v63
	global_store_dword v[54:55], v64, off offset:768
	v_mul_f32_e32 v64, v82, v63
	v_mul_f32_e32 v66, v80, v63
	v_mul_f32_e32 v67, v81, v63
	v_rndne_f32_e32 v65, v65
	v_rndne_f32_e32 v64, v64
	v_cvt_i32_f32_e32 v65, v65
	v_rndne_f32_e32 v66, v66
	v_rndne_f32_e32 v67, v67
	v_cvt_i32_f32_e32 v64, v64
	v_cvt_i32_f32_sdwa v66, v66 dst_sel:WORD_1 dst_unused:UNUSED_PAD src0_sel:DWORD
	v_cvt_i32_f32_e32 v67, v67
	v_lshlrev_b32_e32 v65, 8, v65
	v_and_b32_e32 v65, 0xff00, v65
	v_and_b32_e32 v66, 0xff0000, v66
	v_perm_b32 v64, v67, v64, s25
	v_or3_b32 v64, v64, v65, v66
	v_mul_f32_e32 v65, v93, v63
	global_store_dword v[54:55], v64, off offset:1024
	v_mul_f32_e32 v64, v92, v63
	v_mul_f32_e32 v66, v152, v63
	v_mul_f32_e32 v67, v153, v63
	v_rndne_f32_e32 v65, v65
	v_rndne_f32_e32 v64, v64
	v_cvt_i32_f32_e32 v65, v65
	v_rndne_f32_e32 v66, v66
	v_rndne_f32_e32 v67, v67
	v_cvt_i32_f32_e32 v64, v64
	v_cvt_i32_f32_sdwa v66, v66 dst_sel:WORD_1 dst_unused:UNUSED_PAD src0_sel:DWORD
	v_cvt_i32_f32_e32 v67, v67
	v_lshlrev_b32_e32 v65, 8, v65
	v_and_b32_e32 v65, 0xff00, v65
	v_and_b32_e32 v66, 0xff0000, v66
	v_perm_b32 v64, v67, v64, s25
	v_or3_b32 v64, v64, v65, v66
	v_mul_f32_e32 v65, v137, v63
	global_store_dword v[54:55], v64, off offset:1280
	v_mul_f32_e32 v64, v136, v63
	v_mul_f32_e32 v66, v138, v63
	v_mul_f32_e32 v67, v139, v63
	v_rndne_f32_e32 v65, v65
	v_rndne_f32_e32 v64, v64
	v_cvt_i32_f32_e32 v65, v65
	v_rndne_f32_e32 v66, v66
	v_rndne_f32_e32 v67, v67
	v_cvt_i32_f32_e32 v64, v64
	v_cvt_i32_f32_sdwa v66, v66 dst_sel:WORD_1 dst_unused:UNUSED_PAD src0_sel:DWORD
	v_cvt_i32_f32_e32 v67, v67
	v_lshlrev_b32_e32 v65, 8, v65
	v_and_b32_e32 v65, 0xff00, v65
	v_and_b32_e32 v66, 0xff0000, v66
	v_perm_b32 v64, v67, v64, s25
	v_or3_b32 v64, v64, v65, v66
	v_mul_f32_e32 v65, v141, v63
	global_store_dword v[54:55], v64, off offset:1536
	v_mul_f32_e32 v64, v140, v63
	v_mul_f32_e32 v66, v142, v63
	v_mul_f32_e32 v67, v143, v63
	v_rndne_f32_e32 v65, v65
	v_rndne_f32_e32 v64, v64
	v_cvt_i32_f32_e32 v65, v65
	v_rndne_f32_e32 v66, v66
	v_rndne_f32_e32 v67, v67
	v_cvt_i32_f32_e32 v64, v64
	v_cvt_i32_f32_sdwa v66, v66 dst_sel:WORD_1 dst_unused:UNUSED_PAD src0_sel:DWORD
	v_cvt_i32_f32_e32 v67, v67
	v_lshlrev_b32_e32 v65, 8, v65
	v_and_b32_e32 v65, 0xff00, v65
	v_and_b32_e32 v66, 0xff0000, v66
	v_perm_b32 v64, v67, v64, s25
	v_or3_b32 v64, v64, v65, v66
	v_mul_f32_e32 v65, v145, v63
	global_store_dword v[54:55], v64, off offset:1792
	v_mul_f32_e32 v64, v144, v63
	v_mul_f32_e32 v66, v70, v63
	v_mul_f32_e32 v67, v71, v63
	v_rndne_f32_e32 v65, v65
	v_rndne_f32_e32 v64, v64
	v_cvt_i32_f32_e32 v65, v65
	v_rndne_f32_e32 v66, v66
	v_rndne_f32_e32 v67, v67
	v_cvt_i32_f32_e32 v64, v64
	v_cvt_i32_f32_sdwa v66, v66 dst_sel:WORD_1 dst_unused:UNUSED_PAD src0_sel:DWORD
	v_cvt_i32_f32_e32 v67, v67
	v_lshlrev_b32_e32 v65, 8, v65
	v_and_b32_e32 v65, 0xff00, v65
	v_and_b32_e32 v66, 0xff0000, v66
	v_perm_b32 v64, v67, v64, s25
	v_or3_b32 v64, v64, v65, v66
; __device__ __forceinline__ unsigned pack_i8x4(float a, float b, float c, float d) {
;     const int ia = (int)__builtin_rintf(a), ib = (int)__builtin_rintf(b), ic = (int)__builtin_rintf(c), id = (int)__builtin_rintf(d);
;     return ((unsigned)ia & 255u) | (((unsigned)ib & 255u) << 8) | (((unsigned)ic & 255u) << 16) | ((unsigned)id << 24);
; }
; __device__ __forceinline__ void rms_row_i8_b(const bf16_t* xrow, const float* gain, unsigned char* qrow, float* qscale, int lane) {
;     ...
; #pragma unroll
;     for (int j = 0; j < 16; ++j) ((unsigned*)qrow)[lane + 64 * j] = pack_i8x4(v[j].x * scale, v[j].y * scale, v[j].z * scale, v[j].w * scale);
;     if (lane == 0) *qscale = amax * (1.f / 127.f);
	v_mul_f32_e32 v65, v69, v63
	v_mul_f32_e32 v59, v59, v63
	v_mul_f32_e32 v53, v53, v63
	v_mul_f32_e32 v49, v49, v63
	v_mul_f32_e32 v45, v45, v63
	v_mul_f32_e32 v41, v41, v63
	v_mul_f32_e32 v37, v37, v63
	global_store_dword v[54:55], v64, off offset:2048
	v_mul_f32_e32 v64, v68, v63
	v_mul_f32_e32 v60, v60, v63
	v_mul_f32_e32 v61, v61, v63
	v_rndne_f32_e32 v65, v65
	v_mul_f32_e32 v58, v58, v63
	v_mul_f32_e32 v56, v56, v63
	v_mul_f32_e32 v57, v57, v63
	v_rndne_f32_e32 v59, v59
	v_mul_f32_e32 v52, v52, v63
	v_mul_f32_e32 v50, v50, v63
	v_mul_f32_e32 v51, v51, v63
	v_rndne_f32_e32 v53, v53
	v_mul_f32_e32 v48, v48, v63
	v_mul_f32_e32 v46, v46, v63
	v_mul_f32_e32 v47, v47, v63
	v_rndne_f32_e32 v49, v49
	v_mul_f32_e32 v44, v44, v63
	v_mul_f32_e32 v42, v42, v63
	v_mul_f32_e32 v43, v43, v63
	v_rndne_f32_e32 v45, v45
	v_mul_f32_e32 v40, v40, v63
	v_mul_f32_e32 v38, v38, v63
	v_mul_f32_e32 v39, v39, v63
	v_rndne_f32_e32 v41, v41
	v_mul_f32_e32 v36, v36, v63
	v_mul_f32_e32 v34, v34, v63
	v_mul_f32_e32 v35, v35, v63
	v_rndne_f32_e32 v37, v37
	v_rndne_f32_e32 v64, v64
	v_cvt_i32_f32_e32 v65, v65
	v_rndne_f32_e32 v60, v60
	v_rndne_f32_e32 v61, v61
	v_rndne_f32_e32 v58, v58
	v_cvt_i32_f32_e32 v59, v59
	v_rndne_f32_e32 v56, v56
	v_rndne_f32_e32 v57, v57
	v_rndne_f32_e32 v52, v52
	v_cvt_i32_f32_e32 v53, v53
	v_rndne_f32_e32 v50, v50
	v_rndne_f32_e32 v51, v51
	v_rndne_f32_e32 v48, v48
	v_cvt_i32_f32_e32 v49, v49
	v_rndne_f32_e32 v46, v46
	v_rndne_f32_e32 v47, v47
	v_rndne_f32_e32 v44, v44
	v_cvt_i32_f32_e32 v45, v45
	v_rndne_f32_e32 v42, v42
	v_rndne_f32_e32 v43, v43
	v_rndne_f32_e32 v40, v40
	v_cvt_i32_f32_e32 v41, v41
	v_rndne_f32_e32 v38, v38
	v_rndne_f32_e32 v39, v39
	v_rndne_f32_e32 v36, v36
	v_cvt_i32_f32_e32 v37, v37
	v_rndne_f32_e32 v34, v34
	v_rndne_f32_e32 v35, v35
	v_cvt_i32_f32_e32 v64, v64
	v_cvt_i32_f32_sdwa v60, v60 dst_sel:WORD_1 dst_unused:UNUSED_PAD src0_sel:DWORD
	v_cvt_i32_f32_e32 v61, v61
	v_cvt_i32_f32_e32 v58, v58
	v_cvt_i32_f32_sdwa v56, v56 dst_sel:WORD_1 dst_unused:UNUSED_PAD src0_sel:DWORD
	v_cvt_i32_f32_e32 v57, v57
	v_cvt_i32_f32_e32 v52, v52
	v_cvt_i32_f32_sdwa v50, v50 dst_sel:WORD_1 dst_unused:UNUSED_PAD src0_sel:DWORD
	v_cvt_i32_f32_e32 v51, v51
	v_cvt_i32_f32_e32 v48, v48
	v_cvt_i32_f32_sdwa v46, v46 dst_sel:WORD_1 dst_unused:UNUSED_PAD src0_sel:DWORD
	v_cvt_i32_f32_e32 v47, v47
	v_cvt_i32_f32_e32 v44, v44
	v_cvt_i32_f32_sdwa v42, v42 dst_sel:WORD_1 dst_unused:UNUSED_PAD src0_sel:DWORD
	v_cvt_i32_f32_e32 v43, v43
	v_cvt_i32_f32_e32 v40, v40
	v_cvt_i32_f32_sdwa v38, v38 dst_sel:WORD_1 dst_unused:UNUSED_PAD src0_sel:DWORD
	v_cvt_i32_f32_e32 v39, v39
	v_cvt_i32_f32_e32 v36, v36
	v_cvt_i32_f32_sdwa v34, v34 dst_sel:WORD_1 dst_unused:UNUSED_PAD src0_sel:DWORD
	v_cvt_i32_f32_e32 v35, v35
	v_lshlrev_b32_e32 v65, 8, v65
	v_lshlrev_b32_e32 v59, 8, v59
	v_lshlrev_b32_e32 v53, 8, v53
	v_lshlrev_b32_e32 v49, 8, v49
	v_lshlrev_b32_e32 v45, 8, v45
	v_lshlrev_b32_e32 v41, 8, v41
	v_lshlrev_b32_e32 v37, 8, v37
	v_and_b32_e32 v65, 0xff00, v65
	v_and_b32_e32 v60, 0xff0000, v60
	v_perm_b32 v61, v61, v64, s25
	v_and_b32_e32 v59, 0xff00, v59
	v_and_b32_e32 v56, 0xff0000, v56
	v_perm_b32 v57, v57, v58, s25
	v_and_b32_e32 v53, 0xff00, v53
	v_and_b32_e32 v50, 0xff0000, v50
	v_perm_b32 v51, v51, v52, s25
	v_and_b32_e32 v49, 0xff00, v49
	v_and_b32_e32 v46, 0xff0000, v46
	v_perm_b32 v47, v47, v48, s25
	v_and_b32_e32 v45, 0xff00, v45
	v_and_b32_e32 v42, 0xff0000, v42
	v_perm_b32 v43, v43, v44, s25
	v_and_b32_e32 v41, 0xff00, v41
	v_and_b32_e32 v38, 0xff0000, v38
	v_perm_b32 v39, v39, v40, s25
	v_and_b32_e32 v37, 0xff00, v37
	v_and_b32_e32 v34, 0xff0000, v34
	v_perm_b32 v35, v35, v36, s25
	v_or3_b32 v60, v61, v65, v60
	v_or3_b32 v56, v57, v59, v56
	v_or3_b32 v50, v51, v53, v50
	v_or3_b32 v46, v47, v49, v46
	v_or3_b32 v42, v43, v45, v42
	v_or3_b32 v38, v39, v41, v38
	v_or3_b32 v34, v35, v37, v34
	global_store_dword v[54:55], v60, off offset:2304
	global_store_dword v[54:55], v56, off offset:2560
	global_store_dword v[54:55], v50, off offset:2816
	global_store_dword v[54:55], v46, off offset:3072
	global_store_dword v[54:55], v42, off offset:3328
	global_store_dword v[54:55], v38, off offset:3584
	global_store_dword v[54:55], v34, off offset:3840
	s_and_saveexec_b64 s[8:9], s[6:7]
	s_cbranch_execz .LBB0_1245
	s_add_u32 s28, s88, s22
	v_mul_f32_e32 v34, 0x3c010204, v62
	s_addc_u32 s29, s89, s23
	global_store_dword v3, v34, s[28:29]
	s_branch .LBB0_1245

; __device__ __forceinline__ void rms_row_i8_b(const bf16_t* xrow, const float* gain, unsigned char* qrow, float* qscale, int lane) {
;     const u32x2* xr = (const u32x2*)xrow + lane; const f32x4* gr = (const f32x4*)gain + lane;
; __global__ void __launch_bounds__(NTHREADS, 2) fwd(Args args) {
;     ...
;     if (IN(16)) for (int rep = 0; rep < REPS(16); ++rep) {
;         const int gw14 = F.bid * NWAVES + F.wave, NGW14 = F.G * NWAVES;
;         for (int m = gw14; m < T; m += NGW14) rms_row_i8_b((const bf16_t*)(ws + WS_XB) + (size_t)m * D, args.in[19], ws + WS_D + (size_t)m * D, (float*)(ws + SA_R) + m, F.lane);
.LBB0_1640:
	s_cmp_gt_i32 s90, 16
	s_cselect_b64 s[0:1], -1, 0
	s_cmp_lt_i32 s91, 17
	s_cselect_b64 s[2:3], -1, 0
	s_or_b64 s[0:1], s[0:1], s[2:3]
	s_and_b64 vcc, exec, s[0:1]
	s_cbranch_vccnz .LBB0_1716
	s_lshl_b32 s0, s94, 3
	v_readlane_b32 s1, v245, 7
	s_add_i32 s0, s1, s0
	s_cmpk_gt_i32 s0, 0x1fff
	s_cbranch_scc1 .LBB0_1646
	s_load_dwordx2 s[4:5], s[86:87], 0x98
	v_mbcnt_lo_u32_b32 v1, -1, 0
	s_waitcnt vmcnt(0)
	v_lshlrev_b32_e32 v2, 4, v194
	s_waitcnt lgkmcnt(0)
	v_mov_b32_e32 v3, 0
	v_mbcnt_hi_u32_b32 v30, -1, v1
	v_lshl_add_u64 v[4:5], s[4:5], 0, v[2:3]
	s_mov_b64 s[4:5], 0x1000
	v_and_b32_e32 v1, 64, v30
	v_lshl_add_u64 v[6:7], v[4:5], 0, s[4:5]
	s_mov_b64 s[4:5], 0x1400
	v_add_u32_e32 v31, 64, v1
	v_xor_b32_e32 v1, 1, v30
	v_lshl_add_u64 v[8:9], v[4:5], 0, s[4:5]
	s_mov_b64 s[4:5], 0x1800
	v_cmp_lt_i32_e32 vcc, v1, v31
	v_xor_b32_e32 v2, 2, v30
	v_lshl_add_u64 v[10:11], v[4:5], 0, s[4:5]
	s_mov_b64 s[4:5], 0x1c00
	v_cndmask_b32_e32 v1, v30, v1, vcc
	v_cmp_lt_i32_e32 vcc, v2, v31
	v_xor_b32_e32 v32, 4, v30
	v_lshl_add_u64 v[12:13], v[4:5], 0, s[4:5]
	s_mov_b64 s[4:5], 0x2000
	v_cndmask_b32_e32 v2, v30, v2, vcc
	v_cmp_lt_i32_e32 vcc, v32, v31
	v_lshl_add_u64 v[14:15], v[4:5], 0, s[4:5]
	s_mov_b64 s[4:5], 0x2400
	v_cndmask_b32_e32 v32, v30, v32, vcc
	v_lshl_add_u64 v[16:17], v[4:5], 0, s[4:5]
	s_mov_b64 s[4:5], 0x2800
	v_lshlrev_b32_e32 v106, 2, v32
	v_xor_b32_e32 v32, 8, v30
	v_lshl_add_u64 v[18:19], v[4:5], 0, s[4:5]
	s_mov_b64 s[4:5], 0x2c00
	v_cmp_lt_i32_e32 vcc, v32, v31
	v_lshl_add_u64 v[20:21], v[4:5], 0, s[4:5]
	s_mov_b64 s[4:5], 0x3000
	v_cndmask_b32_e32 v32, v30, v32, vcc
	v_lshl_add_u64 v[22:23], v[4:5], 0, s[4:5]
	s_mov_b64 s[4:5], 0x3400
	v_lshlrev_b32_e32 v107, 2, v32
	v_xor_b32_e32 v32, 16, v30
	v_lshl_add_u64 v[24:25], v[4:5], 0, s[4:5]
	s_mov_b64 s[4:5], 0x3800
	v_cmp_lt_i32_e32 vcc, v32, v31
	v_lshl_add_u64 v[26:27], v[4:5], 0, s[4:5]
	s_mov_b64 s[4:5], 0x3c00
	v_cndmask_b32_e32 v32, v30, v32, vcc
	s_ashr_i32 s1, s0, 31
	s_lshl_b32 s2, s96, 3
	v_lshl_add_u64 v[28:29], v[4:5], 0, s[4:5]
	v_lshlrev_b32_e32 v108, 2, v32
	v_xor_b32_e32 v32, 32, v30
	s_lshl_b64 s[4:5], s[0:1], 2
	v_cmp_lt_i32_e32 vcc, v32, v31
	s_add_u32 s14, s4, 0xf31c000
	s_addc_u32 s15, s5, 0
	v_cndmask_b32_e32 v30, v30, v32, vcc
	s_lshl_b64 s[8:9], s[0:1], 13
	v_lshlrev_b32_e32 v109, 2, v30
	s_ashr_i32 s3, s2, 31
	v_lshl_or_b32 v30, v194, 3, s8
	v_mov_b32_e32 v31, s9
	s_lshl_b64 s[8:9], s[0:1], 12
	v_cmp_eq_u32_e64 s[6:7], 0, v194
	v_lshlrev_b32_e32 v1, 2, v1
	v_lshlrev_b32_e32 v2, 2, v2
	s_lshl_b64 s[4:5], s[2:3], 2
	s_lshl_b64 s[10:11], s[2:3], 13
	v_lshl_or_b32 v32, v194, 2, s8
	v_mov_b32_e32 v33, s9
	s_lshl_b64 s[12:13], s[2:3], 12
	s_mov_b32 s1, 0x13401000
	v_mov_b32_e32 v110, 0x358637bd
	s_mov_b32 s3, 0xf800000
	v_mov_b32_e32 v111, 0x260
	s_mov_b32 s16, 0x42fe0000
	s_mov_b32 s17, 0x40c0c00
	s_mov_b32 s20, 0x33400000
	global_load_dwordx4 v[196:199], v[4:5], off offset:1024
	global_load_dwordx4 v[200:203], v[4:5], off offset:2048
	global_load_dwordx4 v[204:207], v[4:5], off offset:3072
	global_load_dwordx4 v[208:211], v[4:5], off
	global_load_dwordx4 v[212:215], v[6:7], off
	global_load_dwordx4 v[216:219], v[8:9], off
	global_load_dwordx4 v[220:223], v[10:11], off
	global_load_dwordx4 v[224:227], v[12:13], off
	global_load_dwordx4 v[228:231], v[14:15], off
	global_load_dwordx4 v[232:235], v[16:17], off
	global_load_dwordx4 v[236:239], v[18:19], off
	global_load_dwordx4 v[240:243], v[20:21], off
	global_load_dwordx4 v[156:159], v[22:23], off
	global_load_dwordx4 v[160:163], v[24:25], off
	global_load_dwordx4 v[164:167], v[26:27], off
	global_load_dwordx4 v[168:171], v[28:29], off
	s_branch .LBB0_1644

; __device__ __forceinline__ void rms_row_i8_b(const bf16_t* xrow, const float* gain, unsigned char* qrow, float* qscale, int lane) {
;     const u32x2* xr = (const u32x2*)xrow + lane; const f32x4* gr = (const f32x4*)gain + lane;
;     f32x4 v[16]; float s = 0.f;
; #pragma unroll
;     for (int j = 0; j < 16; ++j) { { const u32x2 q = xr[64 * j]; v[j] = (f32x4){bflo(q.x), bfhi(q.x), bflo(q.y), bfhi(q.y)}; } s += (v[j].x * v[j].x + v[j].y * v[j].y) + (v[j].z * v[j].z + v[j].w * v[j].w); }
;     const float rstd = 1.f / sqrtf(wave_sum(s) * (1.f / D) + RMS_EPS);
.LBB0_1644:
	v_lshl_add_u64 v[34:35], s[88:89], 0, v[30:31]
	v_add_co_u32_e32 v36, vcc, 0x13400000, v34
	s_nop 1
	v_addc_co_u32_e32 v37, vcc, 0, v35, vcc
	global_load_dwordx2 v[38:39], v[36:37], off
	global_load_dwordx2 v[40:41], v[36:37], off offset:512
	global_load_dwordx2 v[42:43], v[36:37], off offset:1024
	global_load_dwordx2 v[44:45], v[36:37], off offset:1536
	global_load_dwordx2 v[46:47], v[36:37], off offset:2048
	global_load_dwordx2 v[48:49], v[36:37], off offset:2560
	global_load_dwordx2 v[50:51], v[36:37], off offset:3072
	global_load_dwordx2 v[52:53], v[36:37], off offset:3584
	v_add_co_u32_e32 v34, vcc, s1, v34
	s_waitcnt vmcnt(7)
	v_and_b32_e32 v103, 0xffff0000, v38
	v_addc_co_u32_e32 v35, vcc, 0, v35, vcc
	global_load_dwordx2 v[54:55], v[34:35], off
	global_load_dwordx2 v[56:57], v[34:35], off offset:512
	global_load_dwordx2 v[62:63], v[34:35], off offset:1024
	global_load_dwordx2 v[64:65], v[34:35], off offset:1536
	global_load_dwordx2 v[66:67], v[34:35], off offset:2048
	global_load_dwordx2 v[72:73], v[34:35], off offset:2560
	global_load_dwordx2 v[74:75], v[34:35], off offset:3072
	global_load_dwordx2 v[112:113], v[34:35], off offset:3584
	v_and_b32_e32 v105, 0xffff0000, v39
	v_lshlrev_b32_e32 v102, 16, v38
	v_lshlrev_b32_e32 v104, 16, v39
	s_waitcnt vmcnt(14)
	v_and_b32_e32 v101, 0xffff0000, v41
	v_and_b32_e32 v100, 0xffff0000, v40
	s_waitcnt vmcnt(13)
	v_and_b32_e32 v95, 0xffff0000, v42
	s_waitcnt vmcnt(12)
	v_lshlrev_b32_e32 v93, 16, v44
	s_waitcnt vmcnt(8)
	v_lshlrev_b32_e32 v39, 16, v52
	v_and_b32_e32 v37, 0xffff0000, v52
	v_mul_f32_e32 v36, v105, v105
	v_mul_f32_e32 v38, v103, v103
	v_lshlrev_b32_e32 v99, 16, v41
	v_lshlrev_b32_e32 v98, 16, v40
	v_lshlrev_b32_e32 v94, 16, v42
	v_lshlrev_b32_e32 v96, 16, v43
	v_and_b32_e32 v97, 0xffff0000, v43
	v_and_b32_e32 v91, 0xffff0000, v44
	v_lshlrev_b32_e32 v88, 16, v45
	v_and_b32_e32 v89, 0xffff0000, v45
	v_lshlrev_b32_e32 v81, 16, v47
	v_lshlrev_b32_e32 v80, 16, v46
	v_and_b32_e32 v83, 0xffff0000, v47
	v_and_b32_e32 v82, 0xffff0000, v46
	v_lshlrev_b32_e32 v47, 16, v49
	v_lshlrev_b32_e32 v46, 16, v48
	v_and_b32_e32 v45, 0xffff0000, v49
	v_and_b32_e32 v44, 0xffff0000, v48
	v_lshlrev_b32_e32 v42, 16, v50
	v_and_b32_e32 v43, 0xffff0000, v50
	v_lshlrev_b32_e32 v40, 16, v51
	v_and_b32_e32 v41, 0xffff0000, v51
	v_pk_mul_f32 v[48:49], v[100:101], v[100:101]
	v_mov_b32_e32 v51, v93
	v_mul_f32_e32 v50, v95, v95
	v_pk_fma_f32 v[68:69], v[104:105], v[104:105], v[36:37] op_sel_hi:[1,1,0]
	v_pk_fma_f32 v[70:71], v[102:103], v[102:103], v[38:39] op_sel_hi:[1,1,0]
	v_mul_f32_e32 v52, v97, v97
	v_pk_fma_f32 v[48:49], v[98:99], v[98:99], v[48:49]
	v_pk_fma_f32 v[76:77], v[94:95], v[94:95], v[50:51] op_sel_hi:[1,1,0]
	v_mov_b32_e32 v92, v70
	v_mov_b32_e32 v50, v68
	v_lshlrev_b32_e32 v34, 16, v53
	v_and_b32_e32 v35, 0xffff0000, v53
	v_mul_f32_e32 v78, v91, v91
	v_mul_f32_e32 v79, v88, v88
	v_mul_f32_e32 v84, v89, v89
	v_pk_fma_f32 v[52:53], v[96:97], v[96:97], v[52:53] op_sel_hi:[1,1,0]
	v_pk_add_f32 v[68:69], v[70:71], v[68:69]
	v_pk_add_f32 v[48:49], v[48:49], v[48:49] op_sel:[0,1] op_sel_hi:[1,0]
	v_pk_mul_f32 v[50:51], v[92:93], v[50:51]
	v_mov_b32_e32 v77, v79
	v_mov_b32_e32 v53, v84
	v_mov_b32_e32 v49, v78
	v_mov_b32_e32 v69, v51
	v_pk_mul_f32 v[58:59], v[82:83], v[82:83]
	v_pk_add_f32 v[52:53], v[76:77], v[52:53]
	v_pk_add_f32 v[48:49], v[68:69], v[48:49]
	v_pk_fma_f32 v[58:59], v[80:81], v[80:81], v[58:59]
	v_pk_add_f32 v[48:49], v[48:49], v[52:53]
	v_pk_add_f32 v[58:59], v[58:59], v[58:59] op_sel:[0,1] op_sel_hi:[1,0]
	v_pk_add_f32 v[48:49], v[48:49], v[48:49] op_sel:[0,1] op_sel_hi:[1,0]
	v_pk_mul_f32 v[60:61], v[44:45], v[44:45]
	v_mov_b32_e32 v38, v48
	v_mov_b32_e32 v50, v58
	v_mov_b32_e32 v51, v39
	v_pk_fma_f32 v[60:61], v[46:47], v[46:47], v[60:61]
	v_pk_add_f32 v[48:49], v[48:49], v[58:59]
	v_pk_mul_f32 v[50:51], v[38:39], v[50:51]
	v_mul_f32_e32 v85, v37, v37
	v_mov_b32_e32 v49, v51
	v_pk_add_f32 v[50:51], v[60:61], v[60:61] op_sel:[0,1] op_sel_hi:[1,0]
	v_mul_f32_e32 v36, v43, v43
	v_mov_b32_e32 v51, v85
	v_pk_add_f32 v[48:49], v[48:49], v[50:51]
	v_pk_fma_f32 v[50:51], v[42:43], v[42:43], v[36:37] op_sel_hi:[1,1,0]
	v_mul_f32_e32 v36, v41, v41
	v_mul_f32_e32 v86, v34, v34
	v_mul_f32_e32 v68, v35, v35
	v_pk_fma_f32 v[52:53], v[40:41], v[40:41], v[36:37] op_sel_hi:[1,1,0]
	v_mov_b32_e32 v51, v86
	v_mov_b32_e32 v53, v68
	v_pk_add_f32 v[50:51], v[50:51], v[52:53]
	s_waitcnt vmcnt(7)
	v_and_b32_e32 v71, 0xffff0000, v55
	v_and_b32_e32 v70, 0xffff0000, v54
	v_pk_add_f32 v[76:77], v[48:49], v[50:51]
	v_lshlrev_b32_e32 v69, 16, v55
	v_lshlrev_b32_e32 v68, 16, v54
	v_pk_mul_f32 v[48:49], v[70:71], v[70:71]
	s_waitcnt vmcnt(6)
	v_and_b32_e32 v61, 0xffff0000, v57
	v_pk_fma_f32 v[48:49], v[68:69], v[68:69], v[48:49]
	v_and_b32_e32 v60, 0xffff0000, v56
	v_pk_add_f32 v[78:79], v[48:49], v[48:49] op_sel:[0,1] op_sel_hi:[1,0]
	v_lshlrev_b32_e32 v59, 16, v57
	v_lshlrev_b32_e32 v58, 16, v56
	v_pk_mul_f32 v[48:49], v[60:61], v[60:61]
	s_waitcnt vmcnt(5)
	v_lshlrev_b32_e32 v54, 16, v62
	v_and_b32_e32 v55, 0xffff0000, v62
	v_lshlrev_b32_e32 v56, 16, v63
	v_and_b32_e32 v57, 0xffff0000, v63
	s_waitcnt vmcnt(4)
	v_lshlrev_b32_e32 v53, 16, v64
	v_pk_add_f32 v[62:63], v[76:77], v[76:77] op_sel:[0,1] op_sel_hi:[1,0]
	v_pk_fma_f32 v[84:85], v[58:59], v[58:59], v[48:49]
	v_and_b32_e32 v51, 0xffff0000, v64
	v_lshlrev_b32_e32 v48, 16, v65
	v_and_b32_e32 v49, 0xffff0000, v65
	v_mov_b32_e32 v52, v62
	v_mov_b32_e32 v64, v78
	v_mov_b32_e32 v65, v53
	v_pk_add_f32 v[62:63], v[62:63], v[78:79]
	v_pk_mul_f32 v[64:65], v[52:53], v[64:65]
	v_mul_f32_e32 v36, v51, v51
	v_mov_b32_e32 v63, v65
	v_pk_add_f32 v[64:65], v[84:85], v[84:85] op_sel:[0,1] op_sel_hi:[1,0]
	v_mul_f32_e32 v38, v48, v48
	v_mov_b32_e32 v65, v36
	v_mul_f32_e32 v36, v55, v55
	v_pk_add_f32 v[62:63], v[62:63], v[64:65]
	v_pk_fma_f32 v[64:65], v[54:55], v[54:55], v[36:37] op_sel_hi:[1,1,0]
	v_mul_f32_e32 v36, v57, v57
	v_mul_f32_e32 v50, v49, v49
	v_pk_fma_f32 v[76:77], v[56:57], v[56:57], v[36:37] op_sel_hi:[1,1,0]
	v_mov_b32_e32 v65, v38
	v_mov_b32_e32 v77, v50
	v_pk_add_f32 v[64:65], v[64:65], v[76:77]
	s_waitcnt vmcnt(3)
; __device__ __forceinline__ void rms_row_i8_b(const bf16_t* xrow, const float* gain, unsigned char* qrow, float* qscale, int lane) {
;     ...
;     for (int j = 0; j < 16; ++j) { { const u32x2 q = xr[64 * j]; v[j] = (f32x4){bflo(q.x), bfhi(q.x), bflo(q.y), bfhi(q.y)}; } s += (v[j].x * v[j].x + v[j].y * v[j].y) + (v[j].z * v[j].z + v[j].w * v[j].w); }
;     const float rstd = 1.f / sqrtf(wave_sum(s) * (1.f / D) + RMS_EPS);
;     float amax = 0.f;
; #pragma unroll
;     for (int j = 0; j < 16; ++j) { v[j] = v[j] * rstd * gr[64 * j]; amax = fmaxf(fmaxf(amax, fmaxf(fabsf(v[j].x), fabsf(v[j].y))), fmaxf(fabsf(v[j].z), fabsf(v[j].w))); }
	v_and_b32_e32 v87, 0xffff0000, v67
	v_and_b32_e32 v86, 0xffff0000, v66
	v_pk_add_f32 v[114:115], v[62:63], v[64:65]
	v_lshlrev_b32_e32 v85, 16, v67
	v_lshlrev_b32_e32 v84, 16, v66
	v_pk_mul_f32 v[62:63], v[86:87], v[86:87]
	s_waitcnt vmcnt(2)
	v_and_b32_e32 v79, 0xffff0000, v73
	v_pk_fma_f32 v[62:63], v[84:85], v[84:85], v[62:63]
	v_and_b32_e32 v78, 0xffff0000, v72
	v_pk_add_f32 v[116:117], v[62:63], v[62:63] op_sel:[0,1] op_sel_hi:[1,0]
	v_lshlrev_b32_e32 v77, 16, v73
	v_lshlrev_b32_e32 v76, 16, v72
	v_pk_mul_f32 v[62:63], v[78:79], v[78:79]
	s_waitcnt vmcnt(0)
	v_lshlrev_b32_e32 v67, 16, v112
	v_pk_fma_f32 v[118:119], v[76:77], v[76:77], v[62:63]
	v_and_b32_e32 v65, 0xffff0000, v112
	v_lshlrev_b32_e32 v62, 16, v113
	v_and_b32_e32 v63, 0xffff0000, v113
	v_pk_add_f32 v[112:113], v[114:115], v[114:115] op_sel:[0,1] op_sel_hi:[1,0]
	v_mov_b32_e32 v114, v116
	v_mov_b32_e32 v66, v112
	v_mov_b32_e32 v115, v67
	v_pk_add_f32 v[112:113], v[112:113], v[116:117]
	v_pk_mul_f32 v[114:115], v[66:67], v[114:115]
	v_and_b32_e32 v73, 0xffff0000, v74
	v_mul_f32_e32 v36, v65, v65
	v_mov_b32_e32 v113, v115
	v_pk_add_f32 v[114:115], v[118:119], v[118:119] op_sel:[0,1] op_sel_hi:[1,0]
	v_lshlrev_b32_e32 v72, 16, v74
	v_lshlrev_b32_e32 v74, 16, v75
	v_and_b32_e32 v75, 0xffff0000, v75
	v_mov_b32_e32 v115, v36
	v_mul_f32_e32 v36, v73, v73
	v_pk_add_f32 v[112:113], v[112:113], v[114:115]
	v_pk_fma_f32 v[114:115], v[72:73], v[72:73], v[36:37] op_sel_hi:[1,1,0]
	v_mul_f32_e32 v36, v75, v75
	v_mul_f32_e32 v38, v62, v62
	v_mul_f32_e32 v50, v63, v63
	v_pk_fma_f32 v[116:117], v[74:75], v[74:75], v[36:37] op_sel_hi:[1,1,0]
	v_mov_b32_e32 v115, v38
	v_mov_b32_e32 v117, v50
	v_pk_add_f32 v[114:115], v[114:115], v[116:117]
	v_pk_add_f32 v[112:113], v[112:113], v[114:115]
	v_add_f32_e32 v36, v112, v113
	ds_bpermute_b32 v38, v1, v36
	s_waitcnt lgkmcnt(0)
	v_add_f32_e32 v36, v36, v38
	ds_bpermute_b32 v38, v2, v36
	v_mov_b32_e32 v90, v93
	v_mov_b32_e32 v92, v80
	v_mov_b32_e32 v93, v82
	s_waitcnt lgkmcnt(0)
	v_add_f32_e32 v36, v36, v38
	ds_bpermute_b32 v38, v106, v36
	v_mov_b32_e32 v82, v81
	s_waitcnt lgkmcnt(0)
	v_add_f32_e32 v36, v36, v38
	ds_bpermute_b32 v38, v107, v36
	s_waitcnt lgkmcnt(0)
	v_add_f32_e32 v36, v36, v38
	ds_bpermute_b32 v38, v108, v36
	s_waitcnt lgkmcnt(0)
	v_add_f32_e32 v36, v36, v38
	ds_bpermute_b32 v38, v109, v36
	s_waitcnt lgkmcnt(0)
	v_add_f32_e32 v36, v36, v38
	v_fmamk_f32 v36, v36, 0x39800000, v110
	v_mul_f32_e32 v38, 0x4f800000, v36
	v_cmp_gt_f32_e32 vcc, s3, v36
	s_nop 1
	v_cndmask_b32_e32 v36, v36, v38, vcc
	v_sqrt_f32_e32 v38, v36
	s_nop 0
	v_add_u32_e32 v50, -1, v38
	v_fma_f32 v52, -v50, v38, v36
	v_cmp_ge_f32_e64 s[8:9], 0, v52
	v_add_u32_e32 v52, 1, v38
	s_nop 0
	v_cndmask_b32_e64 v50, v38, v50, s[8:9]
	v_fma_f32 v38, -v52, v38, v36
	v_cmp_lt_f32_e64 s[8:9], 0, v38
	s_nop 1
	v_cndmask_b32_e64 v38, v50, v52, s[8:9]
	v_mul_f32_e32 v50, 0x37800000, v38
	v_cndmask_b32_e32 v38, v38, v50, vcc
	v_cmp_class_f32_e32 vcc, v36, v111
	s_nop 1
	v_cndmask_b32_e32 v36, v38, v36, vcc
	v_div_scale_f32 v38, s[8:9], v36, v36, 1.0
	v_rcp_f32_e32 v50, v38
	s_nop 0
	v_fma_f32 v52, -v38, v50, 1.0
	v_fmac_f32_e32 v50, v52, v50
	v_div_scale_f32 v52, vcc, 1.0, v36, 1.0
	v_mul_f32_e32 v64, v52, v50
	v_fma_f32 v66, -v38, v64, v52
	v_fmac_f32_e32 v64, v66, v50
	v_fma_f32 v38, -v38, v64, v52
	v_div_fmas_f32 v38, v38, v50, v64
	v_div_fixup_f32 v66, v38, v36, 1.0
	v_pk_mul_f32 v[148:149], v[66:67], v[102:103] op_sel_hi:[0,1]
	v_pk_mul_f32 v[102:103], v[66:67], v[104:105] op_sel_hi:[0,1]
	s_waitcnt vmcnt(5)
	v_pk_mul_f32 v[102:103], v[210:211], v[102:103]
	v_pk_mul_f32 v[104:105], v[208:209], v[148:149]
	v_mov_b32_e32 v148, v98
	v_mov_b32_e32 v149, v100
	v_mov_b32_e32 v100, v99
	v_pk_mul_f32 v[148:149], v[66:67], v[148:149] op_sel_hi:[0,1]
	v_pk_mul_f32 v[98:99], v[66:67], v[100:101] op_sel_hi:[0,1]
	v_pk_mul_f32 v[98:99], v[198:199], v[98:99]
	v_pk_mul_f32 v[100:101], v[196:197], v[148:149]
	v_pk_mul_f32 v[148:149], v[66:67], v[94:95] op_sel_hi:[0,1]
	v_pk_mul_f32 v[94:95], v[66:67], v[96:97] op_sel_hi:[0,1]
	v_pk_mul_f32 v[94:95], v[202:203], v[94:95]
	v_pk_mul_f32 v[96:97], v[200:201], v[148:149]
	v_pk_mul_f32 v[90:91], v[90:91], v[66:67] op_sel_hi:[1,0]
	v_pk_mul_f32 v[88:89], v[88:89], v[66:67] op_sel_hi:[1,0]
	v_pk_mul_f32 v[90:91], v[204:205], v[90:91]
	v_pk_mul_f32 v[88:89], v[206:207], v[88:89]
	v_pk_mul_f32 v[92:93], v[66:67], v[92:93] op_sel_hi:[0,1]
	v_pk_mul_f32 v[80:81], v[66:67], v[82:83] op_sel_hi:[0,1]
	s_waitcnt vmcnt(8)
	v_pk_mul_f32 v[80:81], v[214:215], v[80:81]
	v_pk_mul_f32 v[82:83], v[212:213], v[92:93]
	v_mov_b32_e32 v92, v46
	v_mov_b32_e32 v93, v44
	v_mov_b32_e32 v44, v47
	v_pk_mul_f32 v[92:93], v[66:67], v[92:93] op_sel_hi:[0,1]
	v_pk_mul_f32 v[44:45], v[66:67], v[44:45] op_sel_hi:[0,1]
	s_waitcnt vmcnt(9)
	v_pk_mul_f32 v[152:153], v[218:219], v[44:45]
	v_pk_mul_f32 v[92:93], v[216:217], v[92:93]
	v_max_f32_e64 v36, |v104|, |v105|
	v_max_f32_e64 v38, |v102|, |v103|
	v_max3_f32 v36, v36, 0, v38
	v_max_f32_e64 v38, |v100|, |v101|
	v_max_f32_e64 v50, |v98|, |v99|
	v_max3_f32 v36, v36, v38, v50
	v_max_f32_e64 v38, |v96|, |v97|
	v_max_f32_e64 v50, |v94|, |v95|
	v_max3_f32 v36, v36, v38, v50
	v_max_f32_e64 v38, |v90|, |v91|
	v_max_f32_e64 v50, |v88|, |v89|
	v_max3_f32 v36, v36, v38, v50
	v_max_f32_e64 v38, |v82|, |v83|
	v_max_f32_e64 v50, |v80|, |v81|
	v_pk_mul_f32 v[42:43], v[66:67], v[42:43] op_sel_hi:[0,1]
	v_pk_mul_f32 v[40:41], v[66:67], v[40:41] op_sel_hi:[0,1]
	v_max3_f32 v36, v36, v38, v50
	v_max_f32_e64 v38, |v92|, |v93|
	v_max_f32_e64 v44, |v152|, |v153|
	s_waitcnt vmcnt(9)
; __device__ __forceinline__ void rms_row_i8_b(const bf16_t* xrow, const float* gain, unsigned char* qrow, float* qscale, int lane) {
;     ...
;     for (int j = 0; j < 16; ++j) { v[j] = v[j] * rstd * gr[64 * j]; amax = fmaxf(fmaxf(amax, fmaxf(fabsf(v[j].x), fabsf(v[j].y))), fmaxf(fabsf(v[j].z), fabsf(v[j].w))); }
; #pragma unroll
;     for (int o = 1; o < 64; o <<= 1) amax = fmaxf(amax, __shfl_xor(amax, o));
;     const float scale = amax > 0.f ? 127.f / amax : 0.f;
; #pragma unroll
;     for (int j = 0; j < 16; ++j) ((unsigned*)qrow)[lane + 64 * j] = pack_i8x4(v[j].x * scale, v[j].y * scale, v[j].z * scale, v[j].w * scale);
	v_pk_mul_f32 v[138:139], v[222:223], v[40:41]
	v_pk_mul_f32 v[136:137], v[220:221], v[42:43]
	v_max3_f32 v36, v36, v38, v44
	v_max_f32_e64 v38, |v136|, |v137|
	v_max_f32_e64 v40, |v138|, |v139|
	v_max3_f32 v38, v36, v38, v40
	v_mov_b32_e32 v36, v39
	v_pk_mul_f32 v[36:37], v[36:37], v[66:67] op_sel_hi:[1,0]
	v_pk_mul_f32 v[34:35], v[34:35], v[66:67] op_sel_hi:[1,0]
	s_waitcnt vmcnt(8)
	v_pk_mul_f32 v[140:141], v[224:225], v[36:37]
	v_pk_mul_f32 v[142:143], v[226:227], v[34:35]
	v_max_f32_e64 v34, |v140|, |v141|
	v_max_f32_e64 v35, |v142|, |v143|
	v_max3_f32 v38, v38, v34, v35
	v_mov_b32_e32 v34, v68
	v_mov_b32_e32 v35, v70
	v_mov_b32_e32 v70, v69
	v_pk_mul_f32 v[34:35], v[66:67], v[34:35] op_sel_hi:[0,1]
	v_pk_mul_f32 v[36:37], v[66:67], v[70:71] op_sel_hi:[0,1]
	s_waitcnt vmcnt(7)
	v_pk_mul_f32 v[70:71], v[230:231], v[36:37]
	v_pk_mul_f32 v[144:145], v[228:229], v[34:35]
	v_max_f32_e64 v35, |v70|, |v71|
	v_max_f32_e64 v34, |v144|, |v145|
	v_max3_f32 v38, v38, v34, v35
	v_mov_b32_e32 v34, v58
	v_mov_b32_e32 v35, v60
	v_mov_b32_e32 v60, v59
	v_pk_mul_f32 v[34:35], v[66:67], v[34:35] op_sel_hi:[0,1]
	v_pk_mul_f32 v[36:37], v[66:67], v[60:61] op_sel_hi:[0,1]
	s_waitcnt vmcnt(6)
	v_pk_mul_f32 v[60:61], v[234:235], v[36:37]
	v_pk_mul_f32 v[68:69], v[232:233], v[34:35]
	v_max_f32_e64 v35, |v60|, |v61|
	v_max_f32_e64 v34, |v68|, |v69|
	v_max3_f32 v38, v38, v34, v35
	v_pk_mul_f32 v[34:35], v[66:67], v[54:55] op_sel_hi:[0,1]
	v_pk_mul_f32 v[36:37], v[66:67], v[56:57] op_sel_hi:[0,1]
	s_waitcnt vmcnt(5)
	v_pk_mul_f32 v[56:57], v[238:239], v[36:37]
	v_pk_mul_f32 v[58:59], v[236:237], v[34:35]
	v_max_f32_e64 v35, |v56|, |v57|
	v_max_f32_e64 v34, |v58|, |v59|
	v_mov_b32_e32 v50, v53
	v_max3_f32 v38, v38, v34, v35
	v_pk_mul_f32 v[34:35], v[50:51], v[66:67] op_sel_hi:[1,0]
	v_pk_mul_f32 v[36:37], v[48:49], v[66:67] op_sel_hi:[1,0]
	s_waitcnt vmcnt(4)
	v_pk_mul_f32 v[52:53], v[34:35], v[240:241]
	v_pk_mul_f32 v[50:51], v[36:37], v[242:243]
	v_max_f32_e64 v34, |v52|, |v53|
	v_max_f32_e64 v35, |v50|, |v51|
	v_max3_f32 v38, v38, v34, v35
	v_mov_b32_e32 v34, v84
	v_mov_b32_e32 v35, v86
	v_mov_b32_e32 v86, v85
	v_pk_mul_f32 v[34:35], v[66:67], v[34:35] op_sel_hi:[0,1]
	v_pk_mul_f32 v[36:37], v[66:67], v[86:87] op_sel_hi:[0,1]
	s_waitcnt vmcnt(3)
	v_pk_mul_f32 v[46:47], v[36:37], v[158:159]
	v_pk_mul_f32 v[48:49], v[34:35], v[156:157]
	v_max_f32_e64 v35, |v46|, |v47|
	v_max_f32_e64 v34, |v48|, |v49|
	v_max3_f32 v38, v38, v34, v35
	v_mov_b32_e32 v34, v76
	v_mov_b32_e32 v35, v78
	v_mov_b32_e32 v78, v77
	v_pk_mul_f32 v[34:35], v[66:67], v[34:35] op_sel_hi:[0,1]
	v_pk_mul_f32 v[36:37], v[66:67], v[78:79] op_sel_hi:[0,1]
	s_waitcnt vmcnt(2)
	v_pk_mul_f32 v[42:43], v[36:37], v[162:163]
	v_pk_mul_f32 v[44:45], v[34:35], v[160:161]
	v_max_f32_e64 v35, |v42|, |v43|
	v_max_f32_e64 v34, |v44|, |v45|
	v_max3_f32 v54, v38, v34, v35
	v_pk_mul_f32 v[34:35], v[66:67], v[72:73] op_sel_hi:[0,1]
	v_pk_mul_f32 v[36:37], v[66:67], v[74:75] op_sel_hi:[0,1]
	s_waitcnt vmcnt(1)
	v_pk_mul_f32 v[38:39], v[36:37], v[166:167]
	v_pk_mul_f32 v[40:41], v[34:35], v[164:165]
	v_max_f32_e64 v35, |v38|, |v39|
	v_max_f32_e64 v34, |v40|, |v41|
	v_mov_b32_e32 v64, v67
	v_max3_f32 v54, v54, v34, v35
	v_pk_mul_f32 v[36:37], v[64:65], v[66:67] op_sel_hi:[1,0]
	v_pk_mul_f32 v[34:35], v[62:63], v[66:67] op_sel_hi:[1,0]
	s_waitcnt vmcnt(0)
	v_pk_mul_f32 v[36:37], v[36:37], v[168:169]
	v_pk_mul_f32 v[34:35], v[34:35], v[170:171]
	v_max_f32_e64 v55, |v36|, |v37|
	v_max_f32_e64 v62, |v34|, |v35|
	v_max3_f32 v54, v54, v55, v62
	ds_bpermute_b32 v55, v1, v54
	s_waitcnt lgkmcnt(0)
	v_max_f32_e32 v55, v55, v55
	v_max_f32_e32 v54, v54, v55
	ds_bpermute_b32 v55, v2, v54
	s_waitcnt lgkmcnt(0)
	v_max_f32_e32 v55, v55, v55
	v_max_f32_e32 v54, v54, v55
	ds_bpermute_b32 v55, v106, v54
	s_waitcnt lgkmcnt(0)
	v_max_f32_e32 v55, v55, v55
	v_max_f32_e32 v54, v54, v55
	ds_bpermute_b32 v55, v107, v54
	s_waitcnt lgkmcnt(0)
	v_max_f32_e32 v55, v55, v55
	v_max_f32_e32 v54, v54, v55
	ds_bpermute_b32 v55, v108, v54
	s_waitcnt lgkmcnt(0)
	v_max_f32_e32 v55, v55, v55
	v_max_f32_e32 v54, v54, v55
	ds_bpermute_b32 v55, v109, v54
	s_waitcnt lgkmcnt(0)
	v_max_f32_e32 v55, v55, v55
	v_max_f32_e32 v62, v54, v55
	v_div_scale_f32 v54, s[8:9], v62, v62, s16
	v_rcp_f32_e32 v55, v54
	s_nop 0
	v_fma_f32 v63, -v54, v55, 1.0
	v_fmac_f32_e32 v55, v63, v55
	v_div_scale_f32 v63, vcc, s16, v62, s16
	v_mul_f32_e32 v64, v63, v55
	v_fma_f32 v65, -v54, v64, v63
	v_fmac_f32_e32 v64, v65, v55
	v_fma_f32 v54, -v54, v64, v63
	v_div_fmas_f32 v54, v54, v55, v64
	v_div_fixup_f32 v54, v54, v62, s16
	v_cmp_lt_f32_e32 vcc, 0, v62
	s_nop 1
	v_cndmask_b32_e32 v63, 0, v54, vcc
	v_mul_f32_e32 v55, v105, v63
	v_mul_f32_e32 v54, v104, v63
	v_mul_f32_e32 v64, v102, v63
	v_mul_f32_e32 v65, v103, v63
	v_rndne_f32_e32 v55, v55
	v_rndne_f32_e32 v54, v54
	v_cvt_i32_f32_e32 v55, v55
	v_rndne_f32_e32 v64, v64
	v_rndne_f32_e32 v65, v65
	v_cvt_i32_f32_e32 v54, v54
	v_cvt_i32_f32_sdwa v64, v64 dst_sel:WORD_1 dst_unused:UNUSED_PAD src0_sel:DWORD
	v_cvt_i32_f32_e32 v65, v65
	v_lshlrev_b32_e32 v55, 8, v55
	v_and_b32_e32 v55, 0xff00, v55
	v_and_b32_e32 v64, 0xff0000, v64
	v_perm_b32 v54, v65, v54, s17
	v_or3_b32 v64, v54, v55, v64
	v_lshl_add_u64 v[54:55], s[88:89], 0, v[32:33]
	v_add_co_u32_e32 v54, vcc, s20, v54
	v_mul_f32_e32 v65, v101, v63
	s_nop 0
	v_addc_co_u32_e32 v55, vcc, 0, v55, vcc
	global_store_dword v[54:55], v64, off
	v_mul_f32_e32 v64, v100, v63
	v_mul_f32_e32 v66, v98, v63
	v_mul_f32_e32 v67, v99, v63
	v_rndne_f32_e32 v65, v65
	v_rndne_f32_e32 v64, v64
	v_cvt_i32_f32_e32 v65, v65
	v_rndne_f32_e32 v66, v66
	v_rndne_f32_e32 v67, v67
	v_cvt_i32_f32_e32 v64, v64
; __device__ __forceinline__ unsigned pack_i8x4(float a, float b, float c, float d) {
;     const int ia = (int)__builtin_rintf(a), ib = (int)__builtin_rintf(b), ic = (int)__builtin_rintf(c), id = (int)__builtin_rintf(d);
;     return ((unsigned)ia & 255u) | (((unsigned)ib & 255u) << 8) | (((unsigned)ic & 255u) << 16) | ((unsigned)id << 24);
; }
; __device__ __forceinline__ void rms_row_i8_b(const bf16_t* xrow, const float* gain, unsigned char* qrow, float* qscale, int lane) {
;     ...
; #pragma unroll
;     for (int j = 0; j < 16; ++j) ((unsigned*)qrow)[lane + 64 * j] = pack_i8x4(v[j].x * scale, v[j].y * scale, v[j].z * scale, v[j].w * scale);
	v_cvt_i32_f32_sdwa v66, v66 dst_sel:WORD_1 dst_unused:UNUSED_PAD src0_sel:DWORD
	v_cvt_i32_f32_e32 v67, v67
	v_lshlrev_b32_e32 v65, 8, v65
	v_and_b32_e32 v65, 0xff00, v65
	v_and_b32_e32 v66, 0xff0000, v66
	v_perm_b32 v64, v67, v64, s17
	v_or3_b32 v64, v64, v65, v66
	v_mul_f32_e32 v65, v97, v63
	global_store_dword v[54:55], v64, off offset:256
	v_mul_f32_e32 v64, v96, v63
	v_mul_f32_e32 v66, v94, v63
	v_mul_f32_e32 v67, v95, v63
	v_rndne_f32_e32 v65, v65
	v_rndne_f32_e32 v64, v64
	v_cvt_i32_f32_e32 v65, v65
	v_rndne_f32_e32 v66, v66
	v_rndne_f32_e32 v67, v67
	v_cvt_i32_f32_e32 v64, v64
	v_cvt_i32_f32_sdwa v66, v66 dst_sel:WORD_1 dst_unused:UNUSED_PAD src0_sel:DWORD
	v_cvt_i32_f32_e32 v67, v67
	v_lshlrev_b32_e32 v65, 8, v65
	v_and_b32_e32 v65, 0xff00, v65
	v_and_b32_e32 v66, 0xff0000, v66
	v_perm_b32 v64, v67, v64, s17
	v_or3_b32 v64, v64, v65, v66
	v_mul_f32_e32 v65, v91, v63
	global_store_dword v[54:55], v64, off offset:512
	v_mul_f32_e32 v64, v90, v63
	v_mul_f32_e32 v66, v88, v63
	v_mul_f32_e32 v67, v89, v63
	v_rndne_f32_e32 v65, v65
	v_rndne_f32_e32 v64, v64
	v_cvt_i32_f32_e32 v65, v65
	v_rndne_f32_e32 v66, v66
	v_rndne_f32_e32 v67, v67
	v_cvt_i32_f32_e32 v64, v64
	v_cvt_i32_f32_sdwa v66, v66 dst_sel:WORD_1 dst_unused:UNUSED_PAD src0_sel:DWORD
	v_cvt_i32_f32_e32 v67, v67
	v_lshlrev_b32_e32 v65, 8, v65
	v_and_b32_e32 v65, 0xff00, v65
	v_and_b32_e32 v66, 0xff0000, v66
	v_perm_b32 v64, v67, v64, s17
	v_or3_b32 v64, v64, v65, v66
	v_mul_f32_e32 v65, v83, v63
	global_store_dword v[54:55], v64, off offset:768
	v_mul_f32_e32 v64, v82, v63
	v_mul_f32_e32 v66, v80, v63
	v_mul_f32_e32 v67, v81, v63
	v_rndne_f32_e32 v65, v65
	v_rndne_f32_e32 v64, v64
	v_cvt_i32_f32_e32 v65, v65
	v_rndne_f32_e32 v66, v66
	v_rndne_f32_e32 v67, v67
	v_cvt_i32_f32_e32 v64, v64
	v_cvt_i32_f32_sdwa v66, v66 dst_sel:WORD_1 dst_unused:UNUSED_PAD src0_sel:DWORD
	v_cvt_i32_f32_e32 v67, v67
	v_lshlrev_b32_e32 v65, 8, v65
	v_and_b32_e32 v65, 0xff00, v65
	v_and_b32_e32 v66, 0xff0000, v66
	v_perm_b32 v64, v67, v64, s17
	v_or3_b32 v64, v64, v65, v66
	v_mul_f32_e32 v65, v93, v63
	global_store_dword v[54:55], v64, off offset:1024
	v_mul_f32_e32 v64, v92, v63
	v_mul_f32_e32 v66, v152, v63
	v_mul_f32_e32 v67, v153, v63
	v_rndne_f32_e32 v65, v65
	v_rndne_f32_e32 v64, v64
	v_cvt_i32_f32_e32 v65, v65
	v_rndne_f32_e32 v66, v66
	v_rndne_f32_e32 v67, v67
	v_cvt_i32_f32_e32 v64, v64
	v_cvt_i32_f32_sdwa v66, v66 dst_sel:WORD_1 dst_unused:UNUSED_PAD src0_sel:DWORD
	v_cvt_i32_f32_e32 v67, v67
	v_lshlrev_b32_e32 v65, 8, v65
	v_and_b32_e32 v65, 0xff00, v65
	v_and_b32_e32 v66, 0xff0000, v66
	v_perm_b32 v64, v67, v64, s17
	v_or3_b32 v64, v64, v65, v66
	v_mul_f32_e32 v65, v137, v63
	global_store_dword v[54:55], v64, off offset:1280
	v_mul_f32_e32 v64, v136, v63
	v_mul_f32_e32 v66, v138, v63
	v_mul_f32_e32 v67, v139, v63
	v_rndne_f32_e32 v65, v65
	v_rndne_f32_e32 v64, v64
	v_cvt_i32_f32_e32 v65, v65
	v_rndne_f32_e32 v66, v66
	v_rndne_f32_e32 v67, v67
	v_cvt_i32_f32_e32 v64, v64
	v_cvt_i32_f32_sdwa v66, v66 dst_sel:WORD_1 dst_unused:UNUSED_PAD src0_sel:DWORD
	v_cvt_i32_f32_e32 v67, v67
	v_lshlrev_b32_e32 v65, 8, v65
	v_and_b32_e32 v65, 0xff00, v65
	v_and_b32_e32 v66, 0xff0000, v66
	v_perm_b32 v64, v67, v64, s17
	v_or3_b32 v64, v64, v65, v66
	v_mul_f32_e32 v65, v141, v63
	global_store_dword v[54:55], v64, off offset:1536
	v_mul_f32_e32 v64, v140, v63
	v_mul_f32_e32 v66, v142, v63
	v_mul_f32_e32 v67, v143, v63
	v_rndne_f32_e32 v65, v65
	v_rndne_f32_e32 v64, v64
	v_cvt_i32_f32_e32 v65, v65
	v_rndne_f32_e32 v66, v66
	v_rndne_f32_e32 v67, v67
	v_cvt_i32_f32_e32 v64, v64
	v_cvt_i32_f32_sdwa v66, v66 dst_sel:WORD_1 dst_unused:UNUSED_PAD src0_sel:DWORD
	v_cvt_i32_f32_e32 v67, v67
	v_lshlrev_b32_e32 v65, 8, v65
	v_and_b32_e32 v65, 0xff00, v65
	v_and_b32_e32 v66, 0xff0000, v66
	v_perm_b32 v64, v67, v64, s17
	v_or3_b32 v64, v64, v65, v66
	v_mul_f32_e32 v65, v145, v63
	global_store_dword v[54:55], v64, off offset:1792
	v_mul_f32_e32 v64, v144, v63
	v_mul_f32_e32 v66, v70, v63
	v_mul_f32_e32 v67, v71, v63
	v_rndne_f32_e32 v65, v65
	v_rndne_f32_e32 v64, v64
	v_cvt_i32_f32_e32 v65, v65
	v_rndne_f32_e32 v66, v66
	v_rndne_f32_e32 v67, v67
	v_cvt_i32_f32_e32 v64, v64
	v_cvt_i32_f32_sdwa v66, v66 dst_sel:WORD_1 dst_unused:UNUSED_PAD src0_sel:DWORD
	v_cvt_i32_f32_e32 v67, v67
	v_lshlrev_b32_e32 v65, 8, v65
	v_and_b32_e32 v65, 0xff00, v65
	v_and_b32_e32 v66, 0xff0000, v66
	v_perm_b32 v64, v67, v64, s17
	v_or3_b32 v64, v64, v65, v66
; __device__ __forceinline__ unsigned pack_i8x4(float a, float b, float c, float d) {
;     const int ia = (int)__builtin_rintf(a), ib = (int)__builtin_rintf(b), ic = (int)__builtin_rintf(c), id = (int)__builtin_rintf(d);
;     return ((unsigned)ia & 255u) | (((unsigned)ib & 255u) << 8) | (((unsigned)ic & 255u) << 16) | ((unsigned)id << 24);
; }
; __device__ __forceinline__ void rms_row_i8_b(const bf16_t* xrow, const float* gain, unsigned char* qrow, float* qscale, int lane) {
;     ...
; #pragma unroll
;     for (int j = 0; j < 16; ++j) ((unsigned*)qrow)[lane + 64 * j] = pack_i8x4(v[j].x * scale, v[j].y * scale, v[j].z * scale, v[j].w * scale);
;     if (lane == 0) *qscale = amax * (1.f / 127.f);
	v_mul_f32_e32 v65, v69, v63
	v_mul_f32_e32 v59, v59, v63
	v_mul_f32_e32 v53, v53, v63
	v_mul_f32_e32 v49, v49, v63
	v_mul_f32_e32 v45, v45, v63
	v_mul_f32_e32 v41, v41, v63
	v_mul_f32_e32 v37, v37, v63
	global_store_dword v[54:55], v64, off offset:2048
	v_mul_f32_e32 v64, v68, v63
	v_mul_f32_e32 v60, v60, v63
	v_mul_f32_e32 v61, v61, v63
	v_rndne_f32_e32 v65, v65
	v_mul_f32_e32 v58, v58, v63
	v_mul_f32_e32 v56, v56, v63
	v_mul_f32_e32 v57, v57, v63
	v_rndne_f32_e32 v59, v59
	v_mul_f32_e32 v52, v52, v63
	v_mul_f32_e32 v50, v50, v63
	v_mul_f32_e32 v51, v51, v63
	v_rndne_f32_e32 v53, v53
	v_mul_f32_e32 v48, v48, v63
	v_mul_f32_e32 v46, v46, v63
	v_mul_f32_e32 v47, v47, v63
	v_rndne_f32_e32 v49, v49
	v_mul_f32_e32 v44, v44, v63
	v_mul_f32_e32 v42, v42, v63
	v_mul_f32_e32 v43, v43, v63
	v_rndne_f32_e32 v45, v45
	v_mul_f32_e32 v40, v40, v63
	v_mul_f32_e32 v38, v38, v63
	v_mul_f32_e32 v39, v39, v63
	v_rndne_f32_e32 v41, v41
	v_mul_f32_e32 v36, v36, v63
	v_mul_f32_e32 v34, v34, v63
	v_mul_f32_e32 v35, v35, v63
	v_rndne_f32_e32 v37, v37
	v_rndne_f32_e32 v64, v64
	v_cvt_i32_f32_e32 v65, v65
	v_rndne_f32_e32 v60, v60
	v_rndne_f32_e32 v61, v61
	v_rndne_f32_e32 v58, v58
	v_cvt_i32_f32_e32 v59, v59
	v_rndne_f32_e32 v56, v56
	v_rndne_f32_e32 v57, v57
	v_rndne_f32_e32 v52, v52
	v_cvt_i32_f32_e32 v53, v53
	v_rndne_f32_e32 v50, v50
	v_rndne_f32_e32 v51, v51
	v_rndne_f32_e32 v48, v48
	v_cvt_i32_f32_e32 v49, v49
	v_rndne_f32_e32 v46, v46
	v_rndne_f32_e32 v47, v47
	v_rndne_f32_e32 v44, v44
	v_cvt_i32_f32_e32 v45, v45
	v_rndne_f32_e32 v42, v42
	v_rndne_f32_e32 v43, v43
	v_rndne_f32_e32 v40, v40
	v_cvt_i32_f32_e32 v41, v41
	v_rndne_f32_e32 v38, v38
	v_rndne_f32_e32 v39, v39
	v_rndne_f32_e32 v36, v36
	v_cvt_i32_f32_e32 v37, v37
	v_rndne_f32_e32 v34, v34
	v_rndne_f32_e32 v35, v35
	v_cvt_i32_f32_e32 v64, v64
	v_cvt_i32_f32_sdwa v60, v60 dst_sel:WORD_1 dst_unused:UNUSED_PAD src0_sel:DWORD
	v_cvt_i32_f32_e32 v61, v61
	v_cvt_i32_f32_e32 v58, v58
	v_cvt_i32_f32_sdwa v56, v56 dst_sel:WORD_1 dst_unused:UNUSED_PAD src0_sel:DWORD
	v_cvt_i32_f32_e32 v57, v57
	v_cvt_i32_f32_e32 v52, v52
	v_cvt_i32_f32_sdwa v50, v50 dst_sel:WORD_1 dst_unused:UNUSED_PAD src0_sel:DWORD
	v_cvt_i32_f32_e32 v51, v51
	v_cvt_i32_f32_e32 v48, v48
	v_cvt_i32_f32_sdwa v46, v46 dst_sel:WORD_1 dst_unused:UNUSED_PAD src0_sel:DWORD
	v_cvt_i32_f32_e32 v47, v47
	v_cvt_i32_f32_e32 v44, v44
	v_cvt_i32_f32_sdwa v42, v42 dst_sel:WORD_1 dst_unused:UNUSED_PAD src0_sel:DWORD
	v_cvt_i32_f32_e32 v43, v43
	v_cvt_i32_f32_e32 v40, v40
	v_cvt_i32_f32_sdwa v38, v38 dst_sel:WORD_1 dst_unused:UNUSED_PAD src0_sel:DWORD
	v_cvt_i32_f32_e32 v39, v39
	v_cvt_i32_f32_e32 v36, v36
	v_cvt_i32_f32_sdwa v34, v34 dst_sel:WORD_1 dst_unused:UNUSED_PAD src0_sel:DWORD
	v_cvt_i32_f32_e32 v35, v35
	v_lshlrev_b32_e32 v65, 8, v65
	v_lshlrev_b32_e32 v59, 8, v59
	v_lshlrev_b32_e32 v53, 8, v53
	v_lshlrev_b32_e32 v49, 8, v49
	v_lshlrev_b32_e32 v45, 8, v45
	v_lshlrev_b32_e32 v41, 8, v41
	v_lshlrev_b32_e32 v37, 8, v37
	v_and_b32_e32 v65, 0xff00, v65
	v_and_b32_e32 v60, 0xff0000, v60
	v_perm_b32 v61, v61, v64, s17
	v_and_b32_e32 v59, 0xff00, v59
	v_and_b32_e32 v56, 0xff0000, v56
	v_perm_b32 v57, v57, v58, s17
	v_and_b32_e32 v53, 0xff00, v53
	v_and_b32_e32 v50, 0xff0000, v50
	v_perm_b32 v51, v51, v52, s17
	v_and_b32_e32 v49, 0xff00, v49
	v_and_b32_e32 v46, 0xff0000, v46
	v_perm_b32 v47, v47, v48, s17
	v_and_b32_e32 v45, 0xff00, v45
	v_and_b32_e32 v42, 0xff0000, v42
	v_perm_b32 v43, v43, v44, s17
	v_and_b32_e32 v41, 0xff00, v41
	v_and_b32_e32 v38, 0xff0000, v38
	v_perm_b32 v39, v39, v40, s17
	v_and_b32_e32 v37, 0xff00, v37
	v_and_b32_e32 v34, 0xff0000, v34
	v_perm_b32 v35, v35, v36, s17
	v_or3_b32 v60, v61, v65, v60
	v_or3_b32 v56, v57, v59, v56
	v_or3_b32 v50, v51, v53, v50
	v_or3_b32 v46, v47, v49, v46
	v_or3_b32 v42, v43, v45, v42
	v_or3_b32 v38, v39, v41, v38
	v_or3_b32 v34, v35, v37, v34
	global_store_dword v[54:55], v60, off offset:2304
	global_store_dword v[54:55], v56, off offset:2560
	global_store_dword v[54:55], v50, off offset:2816
	global_store_dword v[54:55], v46, off offset:3072
	global_store_dword v[54:55], v42, off offset:3328
	global_store_dword v[54:55], v38, off offset:3584
	global_store_dword v[54:55], v34, off offset:3840
	s_and_saveexec_b64 s[8:9], s[6:7]
	s_cbranch_execz .LBB0_1643
	s_add_u32 s22, s88, s14
	v_mul_f32_e32 v34, 0x3c010204, v62
	s_addc_u32 s23, s89, s15
	global_store_dword v3, v34, s[22:23]
	s_branch .LBB0_1643
